# combined: P0 load batching + out-proj epilogue residual prefetch + gate-up seam counted wait + FoX in-place accumulation
# speedup vs baseline: 1.0085x; 1.0085x over previous
.LBB0_550:
	s_lshl_b32 s5, s23, 13
	s_add_i32 s4, s29, 0xffffff80
	s_cmp_lt_i32 s4, s26
	s_cselect_b64 s[6:7], -1, 0
	s_cmp_gt_i32 s4, s25
	s_cselect_b64 s[8:9], -1, 0
	v_add_u32_e32 v0, s5, v235
	s_or_b64 s[6:7], s[6:7], s[8:9]
	v_add_u32_e32 v215, s5, v236
	s_and_b64 vcc, exec, s[6:7]
	v_add_u32_e32 v245, v0, v232
	v_add_u32_e32 v244, v0, v231
	s_cbranch_vccnz .LBB0_554
	ds_read_b128 v[140:143], v245
	ds_read_b128 v[144:147], v245 offset:512
	ds_read_b128 v[148:151], v244
	ds_read_b128 v[152:155], v244 offset:512
	v_add_u32_e32 v136, v215, v232
	ds_read_b128 v[124:127], v136 offset:16384
	ds_read_b128 v[128:131], v136 offset:18432
	s_waitcnt lgkmcnt(5)
	v_mfma_f32_16x16x32_bf16 v[0:3], v[140:143], v[24:27], 0
	ds_read_b128 v[132:135], v136 offset:20480
	ds_read_b128 v[136:139], v136 offset:22528
	s_add_i32 s5, s29, 31
	s_cmp_le_i32 s5, s22
	s_waitcnt lgkmcnt(6)
	v_mfma_f32_16x16x32_bf16 v[4:7], v[144:147], v[24:27], 0
	s_cselect_b64 s[18:19], -1, 0
	s_mov_b64 s[20:21], -1
	s_and_b64 vcc, exec, s[18:19]
	s_waitcnt lgkmcnt(5)
	v_mfma_f32_16x16x32_bf16 v[156:159], v[148:151], v[28:31], v[0:3]
	s_waitcnt lgkmcnt(4)
	v_mfma_f32_16x16x32_bf16 v[160:163], v[152:155], v[28:31], v[4:7]
	s_cbranch_vccz .LBB0_557
	s_add_i32 s5, s27, 0
	v_mov_b32_e32 v0, s5
	ds_read_b32 v0, v0 offset:49152
	v_cmp_eq_f32_e32 vcc, v242, v233
	s_waitcnt lgkmcnt(0)
	v_sub_f32_e32 v6, v208, v0
	v_pk_fma_f32 v[0:1], v[156:157], s[58:59], v[6:7] op_sel_hi:[1,0,0] neg_lo:[0,0,1] neg_hi:[0,0,1]
	v_pk_fma_f32 v[2:3], v[158:159], s[58:59], v[6:7] op_sel_hi:[1,0,0] neg_lo:[0,0,1] neg_hi:[0,0,1]
	v_pk_fma_f32 v[4:5], v[160:161], s[58:59], v[6:7] op_sel_hi:[1,0,0] neg_lo:[0,0,1] neg_hi:[0,0,1]
	v_pk_fma_f32 v[210:211], v[162:163], s[58:59], v[6:7] op_sel_hi:[1,0,0] neg_lo:[0,0,1] neg_hi:[0,0,1]
	v_max3_f32 v6, v0, v1, v2
	v_max3_f32 v7, v3, v4, v5
	s_nop 0
	v_max3_f32 v164, v210, v211, v211
	s_nop 0
	v_max3_f32 v6, v6, v7, v164
	v_cndmask_b32_e32 v7, v226, v233, vcc
	v_cmp_gt_f32_e32 vcc, v6, v7
	s_cbranch_vccz .LBB0_555
	v_add_f32_e32 v6, v208, v6
	v_mov_b32_e32 v7, v6
	s_nop 1
	v_permlane16_swap_b32 v6, v7
	s_nop 0
	v_max_f32_e32 v7, v7, v7
	v_max_f32_e32 v6, v6, v6
	v_max_f32_e32 v6, v6, v7
	v_mov_b32_e32 v7, v6
	s_nop 1
	v_permlane32_swap_b32 v6, v7
	s_nop 0
	v_max3_f32 v243, v242, v6, v7
	v_cmp_neq_f32_e32 vcc, v243, v233
	s_nop 1
	v_cndmask_b32_e32 v212, 0, v243, vcc
	v_sub_f32_e32 v6, v242, v212
	v_exp_f32_e32 v6, v6
	v_sub_f32_e32 v7, v212, v208
	v_sub_f32_e32 v0, v0, v7
	v_sub_f32_e32 v1, v1, v7
	v_pk_mul_f32 v[110:111], v[110:111], v[6:7] op_sel_hi:[1,0]
	v_pk_mul_f32 v[108:109], v[108:109], v[6:7] op_sel_hi:[1,0]
	v_pk_mul_f32 v[102:103], v[102:103], v[6:7] op_sel_hi:[1,0]
	v_pk_mul_f32 v[100:101], v[100:101], v[6:7] op_sel_hi:[1,0]
	v_pk_mul_f32 v[98:99], v[98:99], v[6:7] op_sel_hi:[1,0]
	v_pk_mul_f32 v[96:97], v[96:97], v[6:7] op_sel_hi:[1,0]
	v_pk_mul_f32 v[94:95], v[94:95], v[6:7] op_sel_hi:[1,0]
	v_pk_mul_f32 v[92:93], v[92:93], v[6:7] op_sel_hi:[1,0]
	v_pk_mul_f32 v[90:91], v[90:91], v[6:7] op_sel_hi:[1,0]
	v_pk_mul_f32 v[88:89], v[88:89], v[6:7] op_sel_hi:[1,0]
	v_sub_f32_e32 v2, v2, v7
	v_sub_f32_e32 v3, v3, v7
	v_sub_f32_e32 v4, v4, v7
	v_sub_f32_e32 v5, v5, v7
	v_sub_f32_e32 v210, v210, v7
	v_sub_f32_e32 v211, v211, v7
	s_branch .LBB0_556

.LBB0_555:
	v_mov_b32_e32 v243, v242
	v_mov_b32_e32 v212, v208

.LBB0_560:
	v_pk_add_f32 v[0:1], v[0:1], v[208:209] op_sel_hi:[1,0] neg_lo:[0,1] neg_hi:[0,1]
	v_pk_add_f32 v[2:3], v[2:3], v[208:209] op_sel_hi:[1,0] neg_lo:[0,1] neg_hi:[0,1]
	v_pk_add_f32 v[4:5], v[4:5], v[208:209] op_sel_hi:[1,0] neg_lo:[0,1] neg_hi:[0,1]
	v_pk_add_f32 v[210:211], v[6:7], v[208:209] op_sel_hi:[1,0] neg_lo:[0,1] neg_hi:[0,1]
	v_exp_f32_e32 v0, v0
	v_exp_f32_e32 v1, v1
	v_exp_f32_e32 v2, v2
	v_exp_f32_e32 v3, v3
	v_exp_f32_e32 v4, v4
	v_exp_f32_e32 v5, v5
	v_exp_f32_e32 v6, v210
	v_mov_b32_e32 v212, v208
	v_mov_b32_e32 v243, v242
.LBB0_561:
	v_exp_f32_e32 v7, v211
	v_cvt_pk_bf16_f32 v0, v0, v1
	v_cvt_pk_bf16_f32 v1, v2, v3
	v_cvt_pk_bf16_f32 v2, v4, v5
	v_cvt_pk_bf16_f32 v3, v6, v7
	s_mov_b64 s[20:21], -1
	s_andn2_b64 vcc, exec, s[18:19]
	v_mfma_f32_16x16x32_bf16 v[108:111], v[112:115], v[0:3], v[108:111]
	s_waitcnt lgkmcnt(3)
	v_mfma_f32_16x16x32_bf16 v[100:103], v[124:127], v[0:3], v[100:103]
	s_waitcnt lgkmcnt(2)
	v_mfma_f32_16x16x32_bf16 v[96:99], v[128:131], v[0:3], v[96:99]
	s_waitcnt lgkmcnt(1)
	v_mfma_f32_16x16x32_bf16 v[92:95], v[132:135], v[0:3], v[92:95]
	s_waitcnt lgkmcnt(0)
	v_mfma_f32_16x16x32_bf16 v[88:91], v[136:139], v[0:3], v[88:91]
	v_mfma_f32_16x16x32_bf16 v[0:3], v[140:143], v[32:35], 0
	v_mfma_f32_16x16x32_bf16 v[148:151], v[148:151], v[36:39], v[0:3]
	v_mfma_f32_16x16x32_bf16 v[0:3], v[144:147], v[32:35], 0
	v_mfma_f32_16x16x32_bf16 v[140:143], v[152:155], v[36:39], v[0:3]
	s_cbranch_vccnz .LBB0_566
	s_add_i32 s5, s27, 0
	s_nop 4
	v_mov_b32_e32 v0, s5
	ds_read_b32 v0, v0 offset:49152
	v_cmp_eq_f32_e32 vcc, v214, v233
	s_waitcnt lgkmcnt(0)
	v_sub_f32_e32 v6, v184, v0
	v_pk_fma_f32 v[0:1], v[148:149], s[58:59], v[6:7] op_sel_hi:[1,0,0] neg_lo:[0,0,1] neg_hi:[0,0,1]
	v_pk_fma_f32 v[2:3], v[150:151], s[58:59], v[6:7] op_sel_hi:[1,0,0] neg_lo:[0,0,1] neg_hi:[0,0,1]
	v_pk_fma_f32 v[4:5], v[140:141], s[58:59], v[6:7] op_sel_hi:[1,0,0] neg_lo:[0,0,1] neg_hi:[0,0,1]
	v_pk_fma_f32 v[168:169], v[142:143], s[58:59], v[6:7] op_sel_hi:[1,0,0] neg_lo:[0,0,1] neg_hi:[0,0,1]
	v_max3_f32 v6, v0, v1, v2
	v_max3_f32 v7, v3, v4, v5
	s_nop 0
	v_max3_f32 v144, v168, v169, v169
	s_nop 0
	v_max3_f32 v6, v6, v7, v144
	v_cndmask_b32_e32 v7, v226, v233, vcc
	v_cmp_gt_f32_e32 vcc, v6, v7
	s_cbranch_vccz .LBB0_564
	v_add_f32_e32 v6, v184, v6
	v_mov_b32_e32 v7, v6
	s_nop 1
	v_permlane16_swap_b32 v6, v7
	s_nop 0
	v_max_f32_e32 v7, v7, v7
	v_max_f32_e32 v6, v6, v6
	v_max_f32_e32 v6, v6, v7
	v_mov_b32_e32 v7, v6
	s_nop 1
	v_permlane32_swap_b32 v7, v6
	s_nop 0
	v_max3_f32 v211, v214, v7, v6
	v_cmp_neq_f32_e32 vcc, v211, v233
	s_nop 1
	v_cndmask_b32_e32 v210, 0, v211, vcc
	v_sub_f32_e32 v6, v214, v210
	v_exp_f32_e32 v6, v6
	v_sub_f32_e32 v7, v210, v184
	v_sub_f32_e32 v0, v0, v7
	v_sub_f32_e32 v1, v1, v7
	v_pk_mul_f32 v[106:107], v[106:107], v[6:7] op_sel_hi:[1,0]
	v_pk_mul_f32 v[104:105], v[104:105], v[6:7] op_sel_hi:[1,0]
	v_pk_mul_f32 v[86:87], v[86:87], v[6:7] op_sel_hi:[1,0]
	v_pk_mul_f32 v[84:85], v[84:85], v[6:7] op_sel_hi:[1,0]
	v_pk_mul_f32 v[82:83], v[82:83], v[6:7] op_sel_hi:[1,0]
	v_pk_mul_f32 v[80:81], v[80:81], v[6:7] op_sel_hi:[1,0]
	v_pk_mul_f32 v[78:79], v[78:79], v[6:7] op_sel_hi:[1,0]
	v_pk_mul_f32 v[76:77], v[76:77], v[6:7] op_sel_hi:[1,0]
	v_pk_mul_f32 v[74:75], v[74:75], v[6:7] op_sel_hi:[1,0]
	v_pk_mul_f32 v[72:73], v[72:73], v[6:7] op_sel_hi:[1,0]
	v_sub_f32_e32 v2, v2, v7
	v_sub_f32_e32 v3, v3, v7
	v_sub_f32_e32 v4, v4, v7
	v_sub_f32_e32 v5, v5, v7
	v_sub_f32_e32 v168, v168, v7
	v_sub_f32_e32 v169, v169, v7
	s_branch .LBB0_565
.LBB0_564:
	v_mov_b32_e32 v211, v214
	v_mov_b32_e32 v210, v184

.LBB0_569:
	v_pk_add_f32 v[0:1], v[0:1], v[184:185] op_sel_hi:[1,0] neg_lo:[0,1] neg_hi:[0,1]
	v_pk_add_f32 v[2:3], v[2:3], v[184:185] op_sel_hi:[1,0] neg_lo:[0,1] neg_hi:[0,1]
	v_pk_add_f32 v[4:5], v[4:5], v[184:185] op_sel_hi:[1,0] neg_lo:[0,1] neg_hi:[0,1]
	v_pk_add_f32 v[168:169], v[6:7], v[184:185] op_sel_hi:[1,0] neg_lo:[0,1] neg_hi:[0,1]
	v_exp_f32_e32 v0, v0
	v_exp_f32_e32 v1, v1
	v_exp_f32_e32 v2, v2
	v_exp_f32_e32 v3, v3
	v_exp_f32_e32 v4, v4
	v_exp_f32_e32 v5, v5
	v_exp_f32_e32 v6, v168
	v_mov_b32_e32 v210, v184
	v_mov_b32_e32 v211, v214
.LBB0_570:
	v_exp_f32_e32 v7, v169
	s_nop 2
	v_cvt_pk_bf16_f32 v0, v0, v1
	v_cvt_pk_bf16_f32 v1, v2, v3
	v_cvt_pk_bf16_f32 v2, v4, v5
	v_cvt_pk_bf16_f32 v3, v6, v7
	s_nop 1
	v_mfma_f32_16x16x32_bf16 v[104:107], v[112:115], v[0:3], v[104:107]
	v_mfma_f32_16x16x32_bf16 v[84:87], v[124:127], v[0:3], v[84:87]
	v_mfma_f32_16x16x32_bf16 v[80:83], v[128:131], v[0:3], v[80:83]
	v_mfma_f32_16x16x32_bf16 v[76:79], v[132:135], v[0:3], v[76:79]
	v_mfma_f32_16x16x32_bf16 v[72:75], v[136:139], v[0:3], v[72:75]
.LBB0_571:
	s_xor_b64 s[10:11], s[10:11], -1
	s_add_i32 s5, s29, 0xffffffa0
	s_cmp_ge_i32 s5, s26
	s_cselect_b64 s[6:7], -1, 0
	s_cmp_lt_i32 s4, s28
	s_cselect_b64 s[4:5], -1, 0
	s_and_b64 s[4:5], s[6:7], s[4:5]
	s_andn2_b64 vcc, exec, s[4:5]
	s_cbranch_vccnz .LBB0_575
	ds_read_b128 v[140:143], v245 offset:4096
	ds_read_b128 v[144:147], v245 offset:4608
	ds_read_b128 v[152:155], v244 offset:4096
	ds_read_b128 v[148:151], v244 offset:4608
	v_add_u32_e32 v136, v215, v231
	ds_read_b128 v[124:127], v136 offset:16384
	ds_read_b128 v[128:131], v136 offset:18432
	ds_read_b128 v[132:135], v136 offset:20480
	ds_read_b128 v[136:139], v136 offset:22528
	s_waitcnt lgkmcnt(7)
	v_mfma_f32_16x16x32_bf16 v[0:3], v[140:143], v[24:27], 0
	s_add_i32 s4, s29, 63
	s_cmp_le_i32 s4, s22
	s_cselect_b64 s[18:19], -1, 0
	s_waitcnt lgkmcnt(6)
	v_mfma_f32_16x16x32_bf16 v[4:7], v[144:147], v[24:27], 0
	s_cmp_gt_i32 s4, s22
	s_mov_b64 s[20:21], -1
	s_waitcnt lgkmcnt(5)
	v_mfma_f32_16x16x32_bf16 v[160:163], v[152:155], v[28:31], v[0:3]
	s_waitcnt lgkmcnt(4)
	v_mfma_f32_16x16x32_bf16 v[156:159], v[148:151], v[28:31], v[4:7]
	s_cbranch_scc1 .LBB0_579
	s_add_i32 s4, s27, 0
	v_mov_b32_e32 v0, s4
	ds_read_b32 v0, v0 offset:49152
	v_cmp_eq_f32_e32 vcc, v243, v233
	s_waitcnt lgkmcnt(0)
	v_sub_f32_e32 v6, v212, v0
	v_pk_fma_f32 v[0:1], v[160:161], s[58:59], v[6:7] op_sel_hi:[1,0,0] neg_lo:[0,0,1] neg_hi:[0,0,1]
	v_pk_fma_f32 v[2:3], v[162:163], s[58:59], v[6:7] op_sel_hi:[1,0,0] neg_lo:[0,0,1] neg_hi:[0,0,1]
	v_pk_fma_f32 v[4:5], v[156:157], s[58:59], v[6:7] op_sel_hi:[1,0,0] neg_lo:[0,0,1] neg_hi:[0,0,1]
	v_pk_fma_f32 v[214:215], v[158:159], s[58:59], v[6:7] op_sel_hi:[1,0,0] neg_lo:[0,0,1] neg_hi:[0,0,1]
	v_max3_f32 v6, v0, v1, v2
	v_max3_f32 v7, v3, v4, v5
	s_nop 0
	v_max3_f32 v164, v214, v215, v215
	s_nop 0
	v_max3_f32 v6, v6, v7, v164
	v_cndmask_b32_e32 v7, v226, v233, vcc
	v_cmp_gt_f32_e32 vcc, v6, v7
	s_cbranch_vccz .LBB0_577
	v_add_f32_e32 v6, v212, v6
	v_mov_b32_e32 v7, v6
	s_nop 1
	v_permlane16_swap_b32 v7, v6
	s_nop 0
	v_max_f32_e32 v6, v6, v6
	v_max_f32_e32 v7, v7, v7
	v_max_f32_e32 v6, v7, v6
	v_mov_b32_e32 v7, v6
	s_nop 1
	v_permlane32_swap_b32 v6, v7
	s_nop 0
	v_max3_f32 v242, v243, v6, v7
	v_cmp_neq_f32_e32 vcc, v242, v233
	s_nop 1
	v_cndmask_b32_e32 v208, 0, v242, vcc
	v_sub_f32_e32 v6, v243, v208
	v_exp_f32_e32 v6, v6
	v_sub_f32_e32 v7, v208, v212
	v_sub_f32_e32 v0, v0, v7
	v_sub_f32_e32 v1, v1, v7
	v_pk_mul_f32 v[110:111], v[110:111], v[6:7] op_sel_hi:[1,0]
	v_pk_mul_f32 v[108:109], v[108:109], v[6:7] op_sel_hi:[1,0]
	v_pk_mul_f32 v[102:103], v[102:103], v[6:7] op_sel_hi:[1,0]
	v_pk_mul_f32 v[100:101], v[100:101], v[6:7] op_sel_hi:[1,0]
	v_pk_mul_f32 v[98:99], v[98:99], v[6:7] op_sel_hi:[1,0]
	v_pk_mul_f32 v[96:97], v[96:97], v[6:7] op_sel_hi:[1,0]
	v_pk_mul_f32 v[94:95], v[94:95], v[6:7] op_sel_hi:[1,0]
	v_pk_mul_f32 v[92:93], v[92:93], v[6:7] op_sel_hi:[1,0]
	v_pk_mul_f32 v[90:91], v[90:91], v[6:7] op_sel_hi:[1,0]
	v_pk_mul_f32 v[88:89], v[88:89], v[6:7] op_sel_hi:[1,0]
	v_sub_f32_e32 v2, v2, v7
	v_sub_f32_e32 v3, v3, v7
	v_sub_f32_e32 v4, v4, v7
	v_sub_f32_e32 v5, v5, v7
	v_sub_f32_e32 v214, v214, v7
	v_sub_f32_e32 v215, v215, v7
	s_branch .LBB0_578

.LBB0_577:
	v_mov_b32_e32 v242, v243
	v_mov_b32_e32 v208, v212

.LBB0_582:
	v_pk_add_f32 v[0:1], v[0:1], v[212:213] op_sel_hi:[1,0] neg_lo:[0,1] neg_hi:[0,1]
	v_pk_add_f32 v[2:3], v[2:3], v[212:213] op_sel_hi:[1,0] neg_lo:[0,1] neg_hi:[0,1]
	v_pk_add_f32 v[4:5], v[4:5], v[212:213] op_sel_hi:[1,0] neg_lo:[0,1] neg_hi:[0,1]
	v_pk_add_f32 v[214:215], v[6:7], v[212:213] op_sel_hi:[1,0] neg_lo:[0,1] neg_hi:[0,1]
	v_exp_f32_e32 v0, v0
	v_exp_f32_e32 v1, v1
	v_exp_f32_e32 v2, v2
	v_exp_f32_e32 v3, v3
	v_exp_f32_e32 v4, v4
	v_exp_f32_e32 v5, v5
	v_exp_f32_e32 v6, v214
	v_mov_b32_e32 v208, v212
	v_mov_b32_e32 v242, v243
.LBB0_583:
	v_exp_f32_e32 v7, v215
	v_cvt_pk_bf16_f32 v0, v0, v1
	v_cvt_pk_bf16_f32 v1, v2, v3
	v_cvt_pk_bf16_f32 v2, v4, v5
	v_cvt_pk_bf16_f32 v3, v6, v7
	s_mov_b64 s[20:21], -1
	s_andn2_b64 vcc, exec, s[18:19]
	v_mfma_f32_16x16x32_bf16 v[108:111], v[112:115], v[0:3], v[108:111]
	s_waitcnt lgkmcnt(3)
	v_mfma_f32_16x16x32_bf16 v[100:103], v[124:127], v[0:3], v[100:103]
	s_waitcnt lgkmcnt(2)
	v_mfma_f32_16x16x32_bf16 v[96:99], v[128:131], v[0:3], v[96:99]
	s_waitcnt lgkmcnt(1)
	v_mfma_f32_16x16x32_bf16 v[92:95], v[132:135], v[0:3], v[92:95]
	s_waitcnt lgkmcnt(0)
	v_mfma_f32_16x16x32_bf16 v[88:91], v[136:139], v[0:3], v[88:91]
	v_mfma_f32_16x16x32_bf16 v[0:3], v[140:143], v[32:35], 0
	v_mfma_f32_16x16x32_bf16 v[152:155], v[152:155], v[36:39], v[0:3]
	v_mfma_f32_16x16x32_bf16 v[0:3], v[144:147], v[32:35], 0
	v_mfma_f32_16x16x32_bf16 v[140:143], v[148:151], v[36:39], v[0:3]
	s_cbranch_vccnz .LBB0_588
	s_add_i32 s4, s27, 0
	s_nop 4
	v_mov_b32_e32 v0, s4
	ds_read_b32 v0, v0 offset:49152
	v_cmp_eq_f32_e32 vcc, v211, v233
	s_waitcnt lgkmcnt(0)
	v_sub_f32_e32 v6, v210, v0
	v_pk_fma_f32 v[0:1], v[152:153], s[58:59], v[6:7] op_sel_hi:[1,0,0] neg_lo:[0,0,1] neg_hi:[0,0,1]
	v_pk_fma_f32 v[2:3], v[154:155], s[58:59], v[6:7] op_sel_hi:[1,0,0] neg_lo:[0,0,1] neg_hi:[0,0,1]
	v_pk_fma_f32 v[4:5], v[140:141], s[58:59], v[6:7] op_sel_hi:[1,0,0] neg_lo:[0,0,1] neg_hi:[0,0,1]
	v_pk_fma_f32 v[168:169], v[142:143], s[58:59], v[6:7] op_sel_hi:[1,0,0] neg_lo:[0,0,1] neg_hi:[0,0,1]
	v_max3_f32 v6, v0, v1, v2
	v_max3_f32 v7, v3, v4, v5
	s_nop 0
	v_max3_f32 v144, v168, v169, v169
	s_nop 0
	v_max3_f32 v6, v6, v7, v144
	v_cndmask_b32_e32 v7, v226, v233, vcc
	v_cmp_gt_f32_e32 vcc, v6, v7
	s_cbranch_vccz .LBB0_586
	v_add_f32_e32 v6, v210, v6
	v_mov_b32_e32 v7, v6
	s_nop 1
	v_permlane16_swap_b32 v6, v7
	s_nop 0
	v_max_f32_e32 v7, v7, v7
	v_max_f32_e32 v6, v6, v6
	v_max_f32_e32 v6, v6, v7
	v_mov_b32_e32 v7, v6
	s_nop 1
	v_permlane32_swap_b32 v7, v6
	s_nop 0
	v_max3_f32 v214, v211, v7, v6
	v_cmp_neq_f32_e32 vcc, v214, v233
	s_nop 1
	v_cndmask_b32_e32 v184, 0, v214, vcc
	v_sub_f32_e32 v6, v211, v184
	v_exp_f32_e32 v6, v6
	v_sub_f32_e32 v7, v184, v210
	v_sub_f32_e32 v0, v0, v7
	v_sub_f32_e32 v1, v1, v7
	v_pk_mul_f32 v[106:107], v[106:107], v[6:7] op_sel_hi:[1,0]
	v_pk_mul_f32 v[104:105], v[104:105], v[6:7] op_sel_hi:[1,0]
	v_pk_mul_f32 v[86:87], v[86:87], v[6:7] op_sel_hi:[1,0]
	v_pk_mul_f32 v[84:85], v[84:85], v[6:7] op_sel_hi:[1,0]
	v_pk_mul_f32 v[82:83], v[82:83], v[6:7] op_sel_hi:[1,0]
	v_pk_mul_f32 v[80:81], v[80:81], v[6:7] op_sel_hi:[1,0]
	v_pk_mul_f32 v[78:79], v[78:79], v[6:7] op_sel_hi:[1,0]
	v_pk_mul_f32 v[76:77], v[76:77], v[6:7] op_sel_hi:[1,0]
	v_pk_mul_f32 v[74:75], v[74:75], v[6:7] op_sel_hi:[1,0]
	v_pk_mul_f32 v[72:73], v[72:73], v[6:7] op_sel_hi:[1,0]
	v_sub_f32_e32 v2, v2, v7
	v_sub_f32_e32 v3, v3, v7
	v_sub_f32_e32 v4, v4, v7
	v_sub_f32_e32 v5, v5, v7
	v_sub_f32_e32 v168, v168, v7
	v_sub_f32_e32 v169, v169, v7
	s_branch .LBB0_587
.LBB0_586:
	v_mov_b32_e32 v214, v211
	v_mov_b32_e32 v184, v210

.LBB0_591:
	v_pk_add_f32 v[0:1], v[0:1], v[210:211] op_sel_hi:[1,0] neg_lo:[0,1] neg_hi:[0,1]
	v_pk_add_f32 v[2:3], v[2:3], v[210:211] op_sel_hi:[1,0] neg_lo:[0,1] neg_hi:[0,1]
	v_pk_add_f32 v[4:5], v[4:5], v[210:211] op_sel_hi:[1,0] neg_lo:[0,1] neg_hi:[0,1]
	v_pk_add_f32 v[168:169], v[6:7], v[210:211] op_sel_hi:[1,0] neg_lo:[0,1] neg_hi:[0,1]
	v_exp_f32_e32 v0, v0
	v_exp_f32_e32 v1, v1
	v_exp_f32_e32 v2, v2
	v_exp_f32_e32 v3, v3
	v_exp_f32_e32 v4, v4
	v_exp_f32_e32 v5, v5
	v_exp_f32_e32 v6, v168
	v_mov_b32_e32 v184, v210
	v_mov_b32_e32 v214, v211
.LBB0_592:
	v_exp_f32_e32 v7, v169
	s_nop 2
	v_cvt_pk_bf16_f32 v0, v0, v1
	v_cvt_pk_bf16_f32 v1, v2, v3
	v_cvt_pk_bf16_f32 v2, v4, v5
	v_cvt_pk_bf16_f32 v3, v6, v7
	s_nop 1
	v_mfma_f32_16x16x32_bf16 v[104:107], v[112:115], v[0:3], v[104:107]
	v_mfma_f32_16x16x32_bf16 v[84:87], v[124:127], v[0:3], v[84:87]
	v_mfma_f32_16x16x32_bf16 v[80:83], v[128:131], v[0:3], v[80:83]
	v_mfma_f32_16x16x32_bf16 v[76:79], v[132:135], v[0:3], v[76:79]
	v_mfma_f32_16x16x32_bf16 v[72:75], v[136:139], v[0:3], v[72:75]
	s_andn2_b64 vcc, exec, s[10:11]
	s_cbranch_vccnz .LBB0_576

.LBB0_754:
	s_mov_b32 s5, s61
	v_mbcnt_lo_u32_b32 v144, -1, 0
	v_mbcnt_hi_u32_b32 v144, -1, v144
	s_lshl_b32 s19, s4, 8
	v_lshl_or_b32 v128, s5, 6, v144
	s_lshl_b32 s5, s24, 8
	v_readfirstlane_b32 s17, v128
	s_lshr_b32 s24, s17, 1
	s_and_b32 s24, s24, 0x60
	s_or_b32 s5, s24, s5
	v_lshrrev_b32_e32 v128, 1, v144
	s_ashr_i32 s4, s4, 3
	v_and_or_b32 v152, v128, 24, s5
	s_mul_hi_i32 s5, s4, 0x6000
	s_mulk_i32 s4, 0x6000
	s_add_u32 s4, s50, s4
	s_addc_u32 s5, s51, s5
	v_ashrrev_i32_e32 v153, 31, v152
	v_lshl_add_u64 v[132:133], v[152:153], 2, s[4:5]
	global_load_dwordx4 v[136:139], v[132:133], off offset:16
	global_load_dwordx4 v[140:143], v[132:133], off
	global_load_dwordx4 v[128:131], v[132:133], off offset:528
	s_nop 0
	global_load_dwordx4 v[132:135], v[132:133], off offset:512
	s_ashr_i32 s4, s17, 2
	s_andn2_b32 s4, s4, 63
	v_lshlrev_b32_e32 v145, 1, v144
	v_and_b32_e32 v145, 24, v145
	v_and_b32_e32 v144, 3, v144
	s_add_i32 s4, s4, s19
	v_or3_b32 v154, s4, v144, v145
	v_ashrrev_i32_e32 v155, 31, v154
	v_lshlrev_b64 v[144:145], 10, v[154:155]
	v_lshl_add_u64 v[156:157], v[144:145], 0, v[152:153]
	v_cndmask_b32_e64 v144, 0, 1, s[14:15]
	v_cmp_ne_u32_e64 s[4:5], 1, v144
	s_andn2_b64 vcc, exec, s[14:15]
	v_lshl_add_u64 v[158:159], v[156:157], 2, s[6:7]
	s_cbranch_vccnz .LBB0_805
	global_load_dwordx4 v[148:151], v[158:159], off offset:16
	global_load_dwordx4 v[144:147], v[158:159], off
	v_lshl_add_u64 v[156:157], v[156:157], 1, s[10:11]
	v_mov_b32_e32 v218, v183
	s_waitcnt vmcnt(0)
	s_cbranch_execnz .LBB0_757
.LBB0_756:
	s_waitcnt vmcnt(15)
	v_lshlrev_b32_e32 v144, 16, v166
	v_and_b32_e32 v145, 0xffff0000, v166
	v_lshlrev_b32_e32 v146, 16, v167
	v_and_b32_e32 v147, 0xffff0000, v167
	v_lshlrev_b32_e32 v148, 16, v168
	v_and_b32_e32 v149, 0xffff0000, v168
	v_lshlrev_b32_e32 v150, 16, v169
	v_and_b32_e32 v151, 0xffff0000, v169
.LBB0_757:
	s_mov_b32 s24, 0x3b000000
	v_pk_mul_f32 v[140:141], v[140:141], s[24:25] op_sel_hi:[1,0]
	v_pk_mul_f32 v[138:139], v[138:139], s[24:25] op_sel_hi:[1,0]
	v_pk_mul_f32 v[136:137], v[136:137], s[24:25] op_sel_hi:[1,0]
	v_pk_mul_f32 v[142:143], v[142:143], s[24:25] op_sel_hi:[1,0]
	v_pk_fma_f32 v[124:125], v[124:125], v[140:141], v[144:145]
	v_pk_fma_f32 v[144:145], v[122:123], v[138:139], v[150:151]
	v_pk_fma_f32 v[122:123], v[120:121], v[136:137], v[148:149]
	s_and_b64 vcc, exec, s[4:5]
	v_pk_fma_f32 v[126:127], v[126:127], v[142:143], v[146:147]
	v_cvt_pk_bf16_f32 v120, v124, v125
	s_nop 0
	v_cvt_pk_bf16_f32 v121, v126, v127
	v_cvt_pk_bf16_f32 v122, v122, v123
	v_cvt_pk_bf16_f32 v123, v144, v145
	global_store_dwordx4 v[156:157], v[120:123], off
	s_cbranch_vccnz .LBB0_806
	global_load_dwordx4 v[124:127], v[158:159], off offset:528
	global_load_dwordx4 v[120:123], v[158:159], off offset:512
	s_waitcnt vmcnt(0)
	s_cbranch_execnz .LBB0_760
.LBB0_759:
	s_waitcnt vmcnt(15)
	v_lshlrev_b32_e32 v120, 16, v170
	v_and_b32_e32 v121, 0xffff0000, v170
	v_lshlrev_b32_e32 v122, 16, v171
	v_and_b32_e32 v123, 0xffff0000, v171
	v_lshlrev_b32_e32 v124, 16, v172
	v_and_b32_e32 v125, 0xffff0000, v172
	v_lshlrev_b32_e32 v126, 16, v173
	v_and_b32_e32 v127, 0xffff0000, v173
.LBB0_760:
	s_mov_b32 s24, 0x3b000000
	v_pk_mul_f32 v[132:133], v[132:133], s[24:25] op_sel_hi:[1,0]
	v_pk_mul_f32 v[130:131], v[130:131], s[24:25] op_sel_hi:[1,0]
	v_pk_mul_f32 v[128:129], v[128:129], s[24:25] op_sel_hi:[1,0]
	v_pk_mul_f32 v[134:135], v[134:135], s[24:25] op_sel_hi:[1,0]
	v_pk_fma_f32 v[116:117], v[116:117], v[132:133], v[120:121]
	v_pk_fma_f32 v[120:121], v[114:115], v[130:131], v[126:127]
	v_pk_fma_f32 v[114:115], v[112:113], v[128:129], v[124:125]
	v_cvt_pk_bf16_f32 v112, v116, v117
	v_pk_fma_f32 v[118:119], v[118:119], v[134:135], v[122:123]
	s_and_b64 vcc, exec, s[4:5]
	v_cvt_pk_bf16_f32 v113, v118, v119
	v_cvt_pk_bf16_f32 v114, v114, v115
	v_cvt_pk_bf16_f32 v115, v120, v121
	global_store_dwordx4 v[156:157], v[112:115], off offset:256
	s_nop 1
	v_or_b32_e32 v112, 4, v154
	v_ashrrev_i32_e32 v113, 31, v112
	v_lshlrev_b64 v[112:113], 10, v[112:113]
	v_lshl_add_u64 v[120:121], v[112:113], 0, v[152:153]
	v_lshl_add_u64 v[122:123], v[120:121], 2, s[6:7]
	s_cbranch_vccnz .LBB0_807
	global_load_dwordx4 v[116:119], v[122:123], off offset:16
	global_load_dwordx4 v[112:115], v[122:123], off
	v_lshl_add_u64 v[120:121], v[120:121], 1, s[10:11]
	s_waitcnt vmcnt(0)
	s_cbranch_execnz .LBB0_763
.LBB0_762:
	s_waitcnt vmcnt(15)
	v_lshlrev_b32_e32 v112, 16, v174
	v_and_b32_e32 v113, 0xffff0000, v174
	v_lshlrev_b32_e32 v114, 16, v175
	v_and_b32_e32 v115, 0xffff0000, v175
	v_lshlrev_b32_e32 v116, 16, v176
	v_and_b32_e32 v117, 0xffff0000, v176
	v_lshlrev_b32_e32 v118, 16, v177
	v_and_b32_e32 v119, 0xffff0000, v177
.LBB0_763:
	v_pk_fma_f32 v[108:109], v[108:109], v[140:141], v[112:113]
	v_pk_fma_f32 v[112:113], v[106:107], v[138:139], v[118:119]
	v_pk_fma_f32 v[106:107], v[104:105], v[136:137], v[116:117]
	s_and_b64 vcc, exec, s[4:5]
	v_pk_fma_f32 v[110:111], v[110:111], v[142:143], v[114:115]
	v_cvt_pk_bf16_f32 v104, v108, v109
	s_nop 0
	v_cvt_pk_bf16_f32 v105, v110, v111
	v_cvt_pk_bf16_f32 v106, v106, v107
	v_cvt_pk_bf16_f32 v107, v112, v113
	global_store_dwordx4 v[120:121], v[104:107], off
	s_cbranch_vccnz .LBB0_808
	global_load_dwordx4 v[108:111], v[122:123], off offset:528
	global_load_dwordx4 v[104:107], v[122:123], off offset:512
	s_waitcnt vmcnt(0)
	s_cbranch_execnz .LBB0_766
.LBB0_765:
	s_waitcnt vmcnt(15)
	v_lshlrev_b32_e32 v104, 16, v178
	v_and_b32_e32 v105, 0xffff0000, v178
	v_lshlrev_b32_e32 v106, 16, v179
	v_and_b32_e32 v107, 0xffff0000, v179
	v_lshlrev_b32_e32 v108, 16, v180
	v_and_b32_e32 v109, 0xffff0000, v180
	v_lshlrev_b32_e32 v110, 16, v181
	v_and_b32_e32 v111, 0xffff0000, v181
.LBB0_766:
	v_pk_fma_f32 v[100:101], v[100:101], v[132:133], v[104:105]
	v_pk_fma_f32 v[104:105], v[98:99], v[130:131], v[110:111]
	v_pk_fma_f32 v[98:99], v[96:97], v[128:129], v[108:109]
	v_cvt_pk_bf16_f32 v96, v100, v101
	v_pk_fma_f32 v[102:103], v[102:103], v[134:135], v[106:107]
	s_and_b64 vcc, exec, s[4:5]
	v_cvt_pk_bf16_f32 v97, v102, v103
	v_cvt_pk_bf16_f32 v98, v98, v99
	v_cvt_pk_bf16_f32 v99, v104, v105
	global_store_dwordx4 v[120:121], v[96:99], off offset:256
	s_nop 1
	v_or_b32_e32 v96, 32, v154
	v_ashrrev_i32_e32 v97, 31, v96
	v_lshlrev_b64 v[96:97], 10, v[96:97]
	v_lshl_add_u64 v[104:105], v[96:97], 0, v[152:153]
	v_lshl_add_u64 v[106:107], v[104:105], 2, s[6:7]
	s_cbranch_vccnz .LBB0_809
	global_load_dwordx4 v[100:103], v[106:107], off offset:16
	global_load_dwordx4 v[96:99], v[106:107], off
	v_lshl_add_u64 v[104:105], v[104:105], 1, s[10:11]
	s_waitcnt vmcnt(0)
	s_cbranch_execnz .LBB0_769
.LBB0_768:
	s_waitcnt vmcnt(15)
	v_lshlrev_b32_e32 v96, 16, v186
	v_and_b32_e32 v97, 0xffff0000, v186
	v_lshlrev_b32_e32 v98, 16, v187
	v_and_b32_e32 v99, 0xffff0000, v187
	v_lshlrev_b32_e32 v100, 16, v188
	v_and_b32_e32 v101, 0xffff0000, v188
	v_lshlrev_b32_e32 v102, 16, v189
	v_and_b32_e32 v103, 0xffff0000, v189
.LBB0_769:
	v_pk_fma_f32 v[92:93], v[92:93], v[140:141], v[96:97]
	v_pk_fma_f32 v[96:97], v[90:91], v[138:139], v[102:103]
	v_pk_fma_f32 v[90:91], v[88:89], v[136:137], v[100:101]
	s_and_b64 vcc, exec, s[4:5]
	v_pk_fma_f32 v[94:95], v[94:95], v[142:143], v[98:99]
	v_cvt_pk_bf16_f32 v88, v92, v93
	s_nop 0
	v_cvt_pk_bf16_f32 v89, v94, v95
	v_cvt_pk_bf16_f32 v90, v90, v91
	v_cvt_pk_bf16_f32 v91, v96, v97
	global_store_dwordx4 v[104:105], v[88:91], off
	s_cbranch_vccnz .LBB0_810
	global_load_dwordx4 v[92:95], v[106:107], off offset:528
	global_load_dwordx4 v[88:91], v[106:107], off offset:512
	s_waitcnt vmcnt(0)
	s_cbranch_execnz .LBB0_772
.LBB0_771:
	s_waitcnt vmcnt(15)
	v_lshlrev_b32_e32 v88, 16, v190
	v_and_b32_e32 v89, 0xffff0000, v190
	v_lshlrev_b32_e32 v90, 16, v191
	v_and_b32_e32 v91, 0xffff0000, v191
	v_lshlrev_b32_e32 v92, 16, v192
	v_and_b32_e32 v93, 0xffff0000, v192
	v_lshlrev_b32_e32 v94, 16, v193
	v_and_b32_e32 v95, 0xffff0000, v193
.LBB0_772:
	v_pk_fma_f32 v[84:85], v[84:85], v[132:133], v[88:89]
	v_pk_fma_f32 v[88:89], v[82:83], v[130:131], v[94:95]
	v_pk_fma_f32 v[82:83], v[80:81], v[128:129], v[92:93]
	v_cvt_pk_bf16_f32 v80, v84, v85
	v_pk_fma_f32 v[86:87], v[86:87], v[134:135], v[90:91]
	s_and_b64 vcc, exec, s[4:5]
	v_cvt_pk_bf16_f32 v81, v86, v87
	v_cvt_pk_bf16_f32 v82, v82, v83
	v_cvt_pk_bf16_f32 v83, v88, v89
	global_store_dwordx4 v[104:105], v[80:83], off offset:256
	s_nop 1
	v_or_b32_e32 v80, 36, v154
	v_ashrrev_i32_e32 v81, 31, v80
	v_lshlrev_b64 v[80:81], 10, v[80:81]
	v_lshl_add_u64 v[88:89], v[80:81], 0, v[152:153]
	v_lshl_add_u64 v[90:91], v[88:89], 2, s[6:7]
	s_cbranch_vccnz .LBB0_811
	global_load_dwordx4 v[84:87], v[90:91], off offset:16
	global_load_dwordx4 v[80:83], v[90:91], off
	v_lshl_add_u64 v[88:89], v[88:89], 1, s[10:11]
	s_waitcnt vmcnt(0)
	s_cbranch_execnz .LBB0_775
.LBB0_774:
	s_waitcnt vmcnt(15)
	v_lshlrev_b32_e32 v80, 16, v194
	v_and_b32_e32 v81, 0xffff0000, v194
	v_lshlrev_b32_e32 v82, 16, v195
	v_and_b32_e32 v83, 0xffff0000, v195
	v_lshlrev_b32_e32 v84, 16, v196
	v_and_b32_e32 v85, 0xffff0000, v196
	v_lshlrev_b32_e32 v86, 16, v197
	v_and_b32_e32 v87, 0xffff0000, v197
.LBB0_775:
	v_pk_fma_f32 v[76:77], v[76:77], v[140:141], v[80:81]
	v_pk_fma_f32 v[80:81], v[74:75], v[138:139], v[86:87]
	v_pk_fma_f32 v[74:75], v[72:73], v[136:137], v[84:85]
	s_and_b64 vcc, exec, s[4:5]
	v_pk_fma_f32 v[78:79], v[78:79], v[142:143], v[82:83]
	v_cvt_pk_bf16_f32 v72, v76, v77
	s_nop 0
	v_cvt_pk_bf16_f32 v73, v78, v79
	v_cvt_pk_bf16_f32 v74, v74, v75
	v_cvt_pk_bf16_f32 v75, v80, v81
	global_store_dwordx4 v[88:89], v[72:75], off
	s_cbranch_vccnz .LBB0_812
	global_load_dwordx4 v[76:79], v[90:91], off offset:528
	global_load_dwordx4 v[72:75], v[90:91], off offset:512
	s_waitcnt vmcnt(0)
	s_cbranch_execnz .LBB0_778
.LBB0_777:
	s_waitcnt vmcnt(15)
	v_lshlrev_b32_e32 v72, 16, v198
	v_and_b32_e32 v73, 0xffff0000, v198
	v_lshlrev_b32_e32 v74, 16, v199
	v_and_b32_e32 v75, 0xffff0000, v199
	v_lshlrev_b32_e32 v76, 16, v200
	v_and_b32_e32 v77, 0xffff0000, v200
	v_lshlrev_b32_e32 v78, 16, v201
	v_and_b32_e32 v79, 0xffff0000, v201
.LBB0_778:
	v_pk_fma_f32 v[68:69], v[68:69], v[132:133], v[72:73]
	v_pk_fma_f32 v[72:73], v[66:67], v[130:131], v[78:79]
	v_pk_fma_f32 v[66:67], v[64:65], v[128:129], v[76:77]
	v_pk_fma_f32 v[70:71], v[70:71], v[134:135], v[74:75]
	v_cvt_pk_bf16_f32 v64, v68, v69
	s_and_b64 vcc, exec, s[4:5]
	v_cvt_pk_bf16_f32 v65, v70, v71
	v_cvt_pk_bf16_f32 v66, v66, v67
	v_cvt_pk_bf16_f32 v67, v72, v73
	v_add_u32_e32 v72, 0x80, v154
	v_ashrrev_i32_e32 v73, 31, v72
	global_store_dwordx4 v[88:89], v[64:67], off offset:256
	s_nop 1
	v_lshlrev_b64 v[64:65], 10, v[72:73]
	v_lshl_add_u64 v[74:75], v[64:65], 0, v[152:153]
	v_lshl_add_u64 v[76:77], v[74:75], 2, s[6:7]
	s_cbranch_vccnz .LBB0_813
	global_load_dwordx4 v[68:71], v[76:77], off offset:16
	global_load_dwordx4 v[64:67], v[76:77], off
	v_lshl_add_u64 v[74:75], v[74:75], 1, s[10:11]
	s_waitcnt vmcnt(0)
	s_cbranch_execnz .LBB0_781
.LBB0_780:
	s_waitcnt vmcnt(15)
	v_lshlrev_b32_e32 v64, 16, v202
	v_and_b32_e32 v65, 0xffff0000, v202
	v_lshlrev_b32_e32 v66, 16, v203
	v_and_b32_e32 v67, 0xffff0000, v203
	v_lshlrev_b32_e32 v68, 16, v204
	v_and_b32_e32 v69, 0xffff0000, v204
	v_lshlrev_b32_e32 v70, 16, v205
	v_and_b32_e32 v71, 0xffff0000, v205
.LBB0_781:
	v_pk_fma_f32 v[60:61], v[60:61], v[140:141], v[64:65]
	v_pk_fma_f32 v[64:65], v[58:59], v[138:139], v[70:71]
	v_pk_fma_f32 v[58:59], v[56:57], v[136:137], v[68:69]
	s_and_b64 vcc, exec, s[4:5]
	v_pk_fma_f32 v[62:63], v[62:63], v[142:143], v[66:67]
	v_cvt_pk_bf16_f32 v56, v60, v61
	s_nop 0
	v_cvt_pk_bf16_f32 v57, v62, v63
	v_cvt_pk_bf16_f32 v58, v58, v59
	v_cvt_pk_bf16_f32 v59, v64, v65
	global_store_dwordx4 v[74:75], v[56:59], off
	s_cbranch_vccnz .LBB0_814
	global_load_dwordx4 v[60:63], v[76:77], off offset:528
	global_load_dwordx4 v[56:59], v[76:77], off offset:512
	s_waitcnt vmcnt(0)
	s_cbranch_execnz .LBB0_784
.LBB0_783:
	s_waitcnt vmcnt(15)
	v_lshlrev_b32_e32 v56, 16, v206
	v_and_b32_e32 v57, 0xffff0000, v206
	v_lshlrev_b32_e32 v58, 16, v207
	v_and_b32_e32 v59, 0xffff0000, v207
	v_lshlrev_b32_e32 v60, 16, v208
	v_and_b32_e32 v61, 0xffff0000, v208
	v_lshlrev_b32_e32 v62, 16, v209
	v_and_b32_e32 v63, 0xffff0000, v209
.LBB0_784:
	v_pk_fma_f32 v[52:53], v[52:53], v[132:133], v[56:57]
	v_pk_fma_f32 v[56:57], v[50:51], v[130:131], v[62:63]
	v_pk_fma_f32 v[50:51], v[48:49], v[128:129], v[60:61]
	v_cvt_pk_bf16_f32 v48, v52, v53
	v_pk_fma_f32 v[54:55], v[54:55], v[134:135], v[58:59]
	s_and_b64 vcc, exec, s[4:5]
	v_cvt_pk_bf16_f32 v49, v54, v55
	v_cvt_pk_bf16_f32 v50, v50, v51
	v_cvt_pk_bf16_f32 v51, v56, v57
	global_store_dwordx4 v[74:75], v[48:51], off offset:256
	s_nop 1
	v_or_b32_e32 v48, 4, v72
	v_ashrrev_i32_e32 v49, 31, v48
	v_lshlrev_b64 v[48:49], 10, v[48:49]
	v_lshl_add_u64 v[56:57], v[48:49], 0, v[152:153]
	v_lshl_add_u64 v[58:59], v[56:57], 2, s[6:7]
	s_cbranch_vccnz .LBB0_815
	global_load_dwordx4 v[52:55], v[58:59], off offset:16
	global_load_dwordx4 v[48:51], v[58:59], off
	v_lshl_add_u64 v[56:57], v[56:57], 1, s[10:11]
	s_waitcnt vmcnt(0)
	s_cbranch_execnz .LBB0_787
.LBB0_786:
	s_waitcnt vmcnt(15)
	v_lshlrev_b32_e32 v48, 16, v210
	v_and_b32_e32 v49, 0xffff0000, v210
	v_lshlrev_b32_e32 v50, 16, v211
	v_and_b32_e32 v51, 0xffff0000, v211
	v_lshlrev_b32_e32 v52, 16, v212
	v_and_b32_e32 v53, 0xffff0000, v212
	v_lshlrev_b32_e32 v54, 16, v213
	v_and_b32_e32 v55, 0xffff0000, v213
.LBB0_787:
	v_pk_fma_f32 v[44:45], v[44:45], v[140:141], v[48:49]
	v_pk_fma_f32 v[48:49], v[42:43], v[138:139], v[54:55]
	v_pk_fma_f32 v[42:43], v[40:41], v[136:137], v[52:53]
	s_and_b64 vcc, exec, s[4:5]
	v_pk_fma_f32 v[46:47], v[46:47], v[142:143], v[50:51]
	v_cvt_pk_bf16_f32 v40, v44, v45
	s_nop 0
	v_cvt_pk_bf16_f32 v41, v46, v47
	v_cvt_pk_bf16_f32 v42, v42, v43
	v_cvt_pk_bf16_f32 v43, v48, v49
	global_store_dwordx4 v[56:57], v[40:43], off
	s_cbranch_vccnz .LBB0_816
	global_load_dwordx4 v[44:47], v[58:59], off offset:528
	global_load_dwordx4 v[40:43], v[58:59], off offset:512
	s_waitcnt vmcnt(0)
	s_cbranch_execnz .LBB0_790
.LBB0_789:
	s_waitcnt vmcnt(15)
	v_lshlrev_b32_e32 v40, 16, v214
	v_and_b32_e32 v41, 0xffff0000, v214
	v_lshlrev_b32_e32 v42, 16, v215
	v_and_b32_e32 v43, 0xffff0000, v215
	v_lshlrev_b32_e32 v44, 16, v216
	v_and_b32_e32 v45, 0xffff0000, v216
	v_lshlrev_b32_e32 v46, 16, v217
	v_and_b32_e32 v47, 0xffff0000, v217
.LBB0_790:
	v_pk_fma_f32 v[36:37], v[36:37], v[132:133], v[40:41]
	v_pk_fma_f32 v[40:41], v[34:35], v[130:131], v[46:47]
	v_pk_fma_f32 v[34:35], v[32:33], v[128:129], v[44:45]
	v_cvt_pk_bf16_f32 v32, v36, v37
	v_pk_fma_f32 v[38:39], v[38:39], v[134:135], v[42:43]
	s_and_b64 vcc, exec, s[4:5]
	v_cvt_pk_bf16_f32 v33, v38, v39
	v_cvt_pk_bf16_f32 v34, v34, v35
	v_cvt_pk_bf16_f32 v35, v40, v41
	global_store_dwordx4 v[56:57], v[32:35], off offset:256
	s_nop 1
	v_or_b32_e32 v32, 32, v72
	v_ashrrev_i32_e32 v33, 31, v32
	v_lshlrev_b64 v[32:33], 10, v[32:33]
	v_lshl_add_u64 v[40:41], v[32:33], 0, v[152:153]
	v_lshl_add_u64 v[42:43], v[40:41], 2, s[6:7]
	s_cbranch_vccnz .LBB0_817
	global_load_dwordx4 v[36:39], v[42:43], off offset:16
	global_load_dwordx4 v[32:35], v[42:43], off
	v_lshl_add_u64 v[40:41], v[40:41], 1, s[10:11]
	s_waitcnt vmcnt(0)
	s_cbranch_execnz .LBB0_793
.LBB0_792:
	s_waitcnt vmcnt(15)
	v_lshlrev_b32_e32 v32, 16, v228
	v_and_b32_e32 v33, 0xffff0000, v228
	v_lshlrev_b32_e32 v34, 16, v229
	v_and_b32_e32 v35, 0xffff0000, v229
	v_lshlrev_b32_e32 v36, 16, v230
	v_and_b32_e32 v37, 0xffff0000, v230
	v_lshlrev_b32_e32 v38, 16, v231
	v_and_b32_e32 v39, 0xffff0000, v231
.LBB0_793:
	v_pk_fma_f32 v[28:29], v[28:29], v[140:141], v[32:33]
	v_pk_fma_f32 v[32:33], v[26:27], v[138:139], v[38:39]
	v_pk_fma_f32 v[26:27], v[24:25], v[136:137], v[36:37]
	s_and_b64 vcc, exec, s[4:5]
	v_pk_fma_f32 v[30:31], v[30:31], v[142:143], v[34:35]
	v_cvt_pk_bf16_f32 v24, v28, v29
	s_nop 0
	v_cvt_pk_bf16_f32 v25, v30, v31
	v_cvt_pk_bf16_f32 v26, v26, v27
	v_cvt_pk_bf16_f32 v27, v32, v33
	global_store_dwordx4 v[40:41], v[24:27], off
	s_cbranch_vccnz .LBB0_818
	global_load_dwordx4 v[28:31], v[42:43], off offset:528
	global_load_dwordx4 v[24:27], v[42:43], off offset:512
	s_waitcnt vmcnt(0)
	s_cbranch_execnz .LBB0_796
.LBB0_795:
	s_waitcnt vmcnt(15)
	v_lshlrev_b32_e32 v24, 16, v232
	v_and_b32_e32 v25, 0xffff0000, v232
	v_lshlrev_b32_e32 v26, 16, v233
	v_and_b32_e32 v27, 0xffff0000, v233
	v_lshlrev_b32_e32 v28, 16, v234
	v_and_b32_e32 v29, 0xffff0000, v234
	v_lshlrev_b32_e32 v30, 16, v235
	v_and_b32_e32 v31, 0xffff0000, v235
.LBB0_796:
	v_pk_fma_f32 v[20:21], v[20:21], v[132:133], v[24:25]
	v_pk_fma_f32 v[24:25], v[18:19], v[130:131], v[30:31]
	v_pk_fma_f32 v[18:19], v[16:17], v[128:129], v[28:29]
	v_cvt_pk_bf16_f32 v16, v20, v21
	v_pk_fma_f32 v[22:23], v[22:23], v[134:135], v[26:27]
	s_and_b64 vcc, exec, s[4:5]
	v_cvt_pk_bf16_f32 v17, v22, v23
	v_cvt_pk_bf16_f32 v18, v18, v19
	v_cvt_pk_bf16_f32 v19, v24, v25
	global_store_dwordx4 v[40:41], v[16:19], off offset:256
	s_nop 1
	v_or_b32_e32 v16, 36, v72
	v_ashrrev_i32_e32 v17, 31, v16
	v_lshlrev_b64 v[16:17], 10, v[16:17]
	v_lshl_add_u64 v[24:25], v[16:17], 0, v[152:153]
	v_lshl_add_u64 v[26:27], v[24:25], 2, s[6:7]
	s_cbranch_vccnz .LBB0_819
	global_load_dwordx4 v[20:23], v[26:27], off offset:16
	global_load_dwordx4 v[16:19], v[26:27], off
	v_lshl_add_u64 v[24:25], v[24:25], 1, s[10:11]
	s_waitcnt vmcnt(0)
	s_cbranch_execnz .LBB0_799
.LBB0_798:
	s_waitcnt vmcnt(15)
	v_lshlrev_b32_e32 v16, 16, v236
	v_and_b32_e32 v17, 0xffff0000, v236
	v_lshlrev_b32_e32 v18, 16, v237
	v_and_b32_e32 v19, 0xffff0000, v237
	v_lshlrev_b32_e32 v20, 16, v238
	v_and_b32_e32 v21, 0xffff0000, v238
	v_lshlrev_b32_e32 v22, 16, v239
	v_and_b32_e32 v23, 0xffff0000, v239
.LBB0_799:
	v_pk_fma_f32 v[12:13], v[12:13], v[140:141], v[16:17]
	v_pk_fma_f32 v[16:17], v[10:11], v[138:139], v[22:23]
	v_pk_fma_f32 v[10:11], v[8:9], v[136:137], v[20:21]
	s_and_b64 vcc, exec, s[4:5]
	v_pk_fma_f32 v[14:15], v[14:15], v[142:143], v[18:19]
	v_cvt_pk_bf16_f32 v8, v12, v13
	s_nop 0
	v_cvt_pk_bf16_f32 v9, v14, v15
	v_cvt_pk_bf16_f32 v10, v10, v11
	v_cvt_pk_bf16_f32 v11, v16, v17
	global_store_dwordx4 v[24:25], v[8:11], off
	s_cbranch_vccnz .LBB0_820
	global_load_dwordx4 v[12:15], v[26:27], off offset:528
	global_load_dwordx4 v[8:11], v[26:27], off offset:512
	s_waitcnt vmcnt(0)
	s_cbranch_execnz .LBB0_802
.LBB0_801:
	s_waitcnt vmcnt(15)
	v_lshlrev_b32_e32 v8, 16, v244
	v_and_b32_e32 v9, 0xffff0000, v244
	v_lshlrev_b32_e32 v10, 16, v245
	v_and_b32_e32 v11, 0xffff0000, v245
	v_lshlrev_b32_e32 v12, 16, v246
	v_and_b32_e32 v13, 0xffff0000, v246
	v_lshlrev_b32_e32 v14, 16, v247
	v_and_b32_e32 v15, 0xffff0000, v247
.LBB0_802:
	v_pk_fma_f32 v[4:5], v[4:5], v[132:133], v[8:9]
	v_pk_fma_f32 v[8:9], v[2:3], v[130:131], v[14:15]
	v_pk_fma_f32 v[2:3], v[0:1], v[128:129], v[12:13]
	v_pk_fma_f32 v[6:7], v[6:7], v[134:135], v[10:11]
	v_cvt_pk_bf16_f32 v0, v4, v5
	s_andn2_b64 vcc, exec, s[2:3]
	v_cvt_pk_bf16_f32 v1, v6, v7
	v_cvt_pk_bf16_f32 v2, v2, v3
	v_cvt_pk_bf16_f32 v3, v8, v9
	s_mov_b64 s[2:3], -1
	global_store_dwordx4 v[24:25], v[0:3], off offset:256
	s_cbranch_vccnz .LBB0_743
	s_nop 0
	v_mov_b32_e32 v0, v185
	s_andn2_b64 vcc, exec, s[8:9]
	s_cbranch_vccnz .LBB0_742
	s_barrier
	s_branch .LBB0_742
.LBB0_805:
	v_lshl_add_u64 v[156:157], v[156:157], 1, s[10:11]
	v_mov_b32_e32 v218, v183
	global_load_dwordx4 v[166:169], v[156:157], off
	global_load_dwordx4 v[170:173], v[156:157], off offset:256
	s_mov_b64 s[78:79], 0x2000
	v_lshl_add_u64 v[250:251], v[156:157], 0, s[78:79]
	global_load_dwordx4 v[174:177], v[250:251], off
	global_load_dwordx4 v[178:181], v[250:251], off offset:256
	s_mov_b64 s[78:79], 0x10000
	v_lshl_add_u64 v[248:249], v[156:157], 0, s[78:79]
	global_load_dwordx4 v[186:189], v[248:249], off
	global_load_dwordx4 v[190:193], v[248:249], off offset:256
	s_mov_b64 s[78:79], 0x12000
	v_lshl_add_u64 v[250:251], v[156:157], 0, s[78:79]
	global_load_dwordx4 v[194:197], v[250:251], off
	global_load_dwordx4 v[198:201], v[250:251], off offset:256
	s_mov_b64 s[78:79], 0x40000
	v_lshl_add_u64 v[248:249], v[156:157], 0, s[78:79]
	global_load_dwordx4 v[202:205], v[248:249], off
	global_load_dwordx4 v[206:209], v[248:249], off offset:256
	s_mov_b64 s[78:79], 0x42000
	v_lshl_add_u64 v[250:251], v[156:157], 0, s[78:79]
	global_load_dwordx4 v[210:213], v[250:251], off
	global_load_dwordx4 v[214:217], v[250:251], off offset:256
	s_mov_b64 s[78:79], 0x50000
	v_lshl_add_u64 v[248:249], v[156:157], 0, s[78:79]
	global_load_dwordx4 v[228:231], v[248:249], off
	global_load_dwordx4 v[232:235], v[248:249], off offset:256
	s_mov_b64 s[78:79], 0x52000
	v_lshl_add_u64 v[250:251], v[156:157], 0, s[78:79]
	global_load_dwordx4 v[236:239], v[250:251], off
	global_load_dwordx4 v[244:247], v[250:251], off offset:256
	s_branch .LBB0_756

.LBB0_1041:
	s_ashr_i32 s29, s28, 31
	s_lshl_b64 s[24:25], s[28:29], 2
	s_add_u32 s24, s38, s24
	s_addc_u32 s25, s39, s25
	v_mov_b32_e32 v40, v152
	global_load_dword v155, v185, s[24:25]
	s_lshl_b32 s19, s28, 8
	v_lshrrev_b32_e32 v40, 10, v40
	v_add_u32_e32 v40, s19, v40
	v_ashrrev_i32_e32 v41, 31, v40
	v_lshl_add_u64 v[40:41], v[40:41], 2, s[6:7]
	global_load_dword v156, v[40:41], off
	v_mov_b32_e32 v40, v153
	s_nop 0
	v_lshrrev_b32_e32 v40, 10, v40
	v_add_u32_e32 v40, s19, v40
	v_ashrrev_i32_e32 v41, 31, v40
	v_lshl_add_u64 v[40:41], v[40:41], 2, s[6:7]
	global_load_dword v157, v[40:41], off
	v_mov_b32_e32 v40, v152
	s_bitset1_b32 s19, 7
	v_lshrrev_b32_e32 v40, 10, v40
	v_add_u32_e32 v40, s19, v40
	v_ashrrev_i32_e32 v41, 31, v40
	v_lshl_add_u64 v[40:41], v[40:41], 2, s[6:7]
	global_load_dword v158, v[40:41], off
	v_mov_b32_e32 v40, v153
	s_nop 0
	v_lshrrev_b32_e32 v40, 10, v40
	v_add_u32_e32 v40, s19, v40
	v_ashrrev_i32_e32 v41, 31, v40
	v_lshl_add_u64 v[40:41], v[40:41], 2, s[6:7]
	s_mov_b32 s19, s61
	global_load_dword v159, v[40:41], off
	v_mbcnt_lo_u32_b32 v40, -1, 0
	v_mbcnt_hi_u32_b32 v40, -1, v40
	s_lshl_b32 s19, s19, 6
	v_mov_b32_e32 v41, 0xff
	v_bitop3_b32 v40, s19, v41, v40 bitop3:0xc8
	s_movk_i32 s19, 0x80
	v_cmp_gt_u32_e32 vcc, s19, v40
	s_lshl_b32 s19, s26, 7
	v_or_b32_e32 v41, s19, v40
	s_addk_i32 s19, 0x380
	v_add_u32_e32 v40, s19, v40
	s_ashr_i32 s19, s18, 31
	s_lshl_b64 s[24:25], s[18:19], 13
	v_cndmask_b32_e32 v40, v40, v41, vcc
	s_add_u32 s24, s68, s24
	v_ashrrev_i32_e32 v41, 31, v40
	s_addc_u32 s25, s70, s25
	v_lshl_add_u64 v[40:41], v[40:41], 2, s[24:25]
	s_mov_b32 s19, s61
	global_load_dword v160, v[40:41], off
	v_mbcnt_lo_u32_b32 v161, -1, 0
	v_mbcnt_hi_u32_b32 v161, -1, v161
	s_lshl_b32 s24, s72, 10
	v_lshl_or_b32 v40, s19, 6, v161
	s_and_b32 s24, s24, 0x400
	v_readfirstlane_b32 s19, v40
	s_lshr_b32 s25, s19, 1
	s_and_b32 s25, s25, 0x60
	s_add_i32 s24, s24, 0
	s_lshl_b32 s29, s25, 2
	s_add_i32 s24, s24, s29
	s_lshl_b32 s29, s34, 7
	v_lshrrev_b32_e32 v40, 1, v161
	v_lshlrev_b32_e32 v163, 1, v161
	v_and_or_b32 v162, v40, 16, s29
	v_and_b32_e32 v40, 0x60, v163
	v_add_u32_e32 v40, s24, v40
	v_add_u32_e32 v140, 0x23000, v40
	ds_read_b128 v[52:55], v140
	ds_read_b128 v[40:43], v140 offset:16
	ds_read_b128 v[136:139], v140 offset:512
	s_lshl_b32 s24, s30, 8
	s_mov_b32 s30, 0xc01d265f
	s_waitcnt lgkmcnt(0)
	v_pk_fma_f32 v[132:133], v[132:133], s[48:49], v[52:53] op_sel_hi:[1,0,1]
	s_ashr_i32 s19, s19, 2
	v_pk_fma_f32 v[144:145], v[138:139], 4.0, 4.0 op_sel_hi:[1,0,0]
	v_pk_fma_f32 v[146:147], v[136:137], 4.0, 4.0 op_sel_hi:[1,0,0]
	ds_read_b128 v[136:139], v140 offset:528
	v_min_f32_e32 v132, 0x40e00000, v132
	v_min_f32_e32 v133, 0x40e00000, v133
	s_andn2_b32 s19, s19, 63
	s_add_i32 s19, s19, s24
	s_waitcnt lgkmcnt(0)
	v_pk_fma_f32 v[142:143], v[138:139], 4.0, 4.0 op_sel_hi:[1,0,0]
	v_and_b32_e32 v138, 3, v161
	v_pk_fma_f32 v[140:141], v[136:137], 4.0, 4.0 op_sel_hi:[1,0,0]
	v_or_b32_e32 v136, s25, v162
	v_and_or_b32 v138, v163, 24, v138
	v_pk_mul_f32 v[162:163], v[132:133], s[30:31] op_sel_hi:[1,0]
	v_lshrrev_b32_e32 v137, 2, v161
	v_exp_f32_e32 v162, v162
	v_exp_f32_e32 v163, v163
	v_and_b32_e32 v137, 4, v137
	s_mov_b32 s24, 0x3d800000
	v_or3_b32 v138, v138, v137, s19
	v_pk_add_f32 v[162:163], v[162:163], 1.0 op_sel_hi:[1,0]
	v_pk_fma_f32 v[128:129], v[128:129], s[24:25], v[146:147] op_sel_hi:[1,0,1]
	v_rcp_f32_e32 v162, v162
	v_rcp_f32_e32 v163, v163
	s_mov_b32 s19, 0xc1c00000
	v_mov_b32_e32 v161, 0x42000000
	v_pk_fma_f32 v[134:135], v[134:135], s[48:49], v[54:55] op_sel_hi:[1,0,1]
	v_med3_f32 v128, v128, s19, v161
	v_med3_f32 v129, v129, s19, v161
	v_pk_mul_f32 v[132:133], v[132:133], v[162:163]
	v_pk_fma_f32 v[130:131], v[130:131], s[24:25], v[144:145] op_sel_hi:[1,0,1]
	v_pk_mul_f32 v[132:133], v[128:129], v[132:133]
	v_min_f32_e32 v128, 0x40e00000, v134
	v_min_f32_e32 v129, 0x40e00000, v135
	v_pk_mul_f32 v[134:135], v[128:129], s[30:31] op_sel_hi:[1,0]
	v_med3_f32 v130, v130, s19, v161
	v_exp_f32_e32 v134, v134
	v_exp_f32_e32 v135, v135
	v_med3_f32 v131, v131, s19, v161
	v_pk_fma_f32 v[124:125], v[124:125], s[48:49], v[40:41] op_sel_hi:[1,0,1]
	v_pk_fma_f32 v[120:121], v[120:121], s[24:25], v[140:141] op_sel_hi:[1,0,1]
	v_pk_add_f32 v[134:135], v[134:135], 1.0 op_sel_hi:[1,0]
	v_min_f32_e32 v124, 0x40e00000, v124
	v_rcp_f32_e32 v134, v134
	v_rcp_f32_e32 v135, v135
	v_min_f32_e32 v125, 0x40e00000, v125
	v_med3_f32 v120, v120, s19, v161
	v_med3_f32 v121, v121, s19, v161
	v_pk_mul_f32 v[128:129], v[128:129], v[134:135]
	v_pk_fma_f32 v[116:117], v[116:117], s[48:49], v[52:53] op_sel_hi:[1,0,1]
	v_pk_mul_f32 v[130:131], v[130:131], v[128:129]
	v_mov_b32_e32 v128, v185
	v_cvt_pk_fp8_f32 v128, v132, v133
	v_mov_b32_e32 v129, v185
	v_min_f32_e32 v116, 0x40e00000, v116
	v_min_f32_e32 v117, 0x40e00000, v117
	v_cvt_pk_fp8_f32 v128, v130, v131 op_sel:[0,0,1]
	v_pk_mul_f32 v[130:131], v[124:125], s[30:31] op_sel_hi:[1,0]
	v_pk_fma_f32 v[112:113], v[112:113], s[24:25], v[146:147] op_sel_hi:[1,0,1]
	v_exp_f32_e32 v130, v130
	v_exp_f32_e32 v131, v131
	v_med3_f32 v112, v112, s19, v161
	v_med3_f32 v113, v113, s19, v161
	v_pk_fma_f32 v[108:109], v[108:109], s[48:49], v[40:41] op_sel_hi:[1,0,1]
	v_pk_add_f32 v[130:131], v[130:131], 1.0 op_sel_hi:[1,0]
	v_min_f32_e32 v108, 0x40e00000, v108
	v_rcp_f32_e32 v130, v130
	v_rcp_f32_e32 v131, v131
	v_min_f32_e32 v109, 0x40e00000, v109
	v_pk_fma_f32 v[104:105], v[104:105], s[24:25], v[140:141] op_sel_hi:[1,0,1]
	v_pk_fma_f32 v[126:127], v[126:127], s[48:49], v[42:43] op_sel_hi:[1,0,1]
	v_pk_mul_f32 v[124:125], v[124:125], v[130:131]
	v_mov_b32_e32 v130, v185
	v_pk_mul_f32 v[120:121], v[120:121], v[124:125]
	v_pk_fma_f32 v[118:119], v[118:119], s[48:49], v[54:55] op_sel_hi:[1,0,1]
	v_cvt_pk_fp8_f32 v129, v120, v121
	v_pk_mul_f32 v[120:121], v[116:117], s[30:31] op_sel_hi:[1,0]
	v_pk_fma_f32 v[110:111], v[110:111], s[48:49], v[42:43] op_sel_hi:[1,0,1]
	v_exp_f32_e32 v120, v120
	v_exp_f32_e32 v121, v121
	v_med3_f32 v104, v104, s19, v161
	v_med3_f32 v105, v105, s19, v161
	v_min_f32_e32 v124, 0x40e00000, v126
	v_pk_add_f32 v[120:121], v[120:121], 1.0 op_sel_hi:[1,0]
	v_min_f32_e32 v125, 0x40e00000, v127
	v_rcp_f32_e32 v120, v120
	v_rcp_f32_e32 v121, v121
	v_pk_mul_f32 v[126:127], v[124:125], s[30:31] op_sel_hi:[1,0]
	v_mov_b32_e32 v131, v185
	v_exp_f32_e32 v126, v126
	v_pk_mul_f32 v[116:117], v[116:117], v[120:121]
	v_exp_f32_e32 v127, v127
	v_pk_mul_f32 v[112:113], v[112:113], v[116:117]
	v_min_f32_e32 v116, 0x40e00000, v118
	v_cvt_pk_fp8_f32 v130, v112, v113
	v_pk_mul_f32 v[112:113], v[108:109], s[30:31] op_sel_hi:[1,0]
	v_min_f32_e32 v117, 0x40e00000, v119
	v_exp_f32_e32 v112, v112
	v_exp_f32_e32 v113, v113
	v_pk_mul_f32 v[118:119], v[116:117], s[30:31] op_sel_hi:[1,0]
	v_pk_add_f32 v[126:127], v[126:127], 1.0 op_sel_hi:[1,0]
	v_exp_f32_e32 v118, v118
	v_pk_add_f32 v[112:113], v[112:113], 1.0 op_sel_hi:[1,0]
	v_exp_f32_e32 v119, v119
	v_rcp_f32_e32 v112, v112
	v_rcp_f32_e32 v113, v113
	v_rcp_f32_e32 v126, v126
	v_pk_add_f32 v[118:119], v[118:119], 1.0 op_sel_hi:[1,0]
	v_rcp_f32_e32 v127, v127
	v_pk_mul_f32 v[108:109], v[108:109], v[112:113]
	v_rcp_f32_e32 v118, v118
	v_pk_mul_f32 v[104:105], v[104:105], v[108:109]
	v_min_f32_e32 v108, 0x40e00000, v110
	v_min_f32_e32 v109, 0x40e00000, v111
	v_pk_mul_f32 v[110:111], v[108:109], s[30:31] op_sel_hi:[1,0]
	v_rcp_f32_e32 v119, v119
	v_exp_f32_e32 v110, v110
	v_exp_f32_e32 v111, v111
	v_cvt_pk_fp8_f32 v131, v104, v105
	v_pk_fma_f32 v[122:123], v[122:123], s[24:25], v[142:143] op_sel_hi:[1,0,1]
	v_pk_fma_f32 v[114:115], v[114:115], s[24:25], v[144:145] op_sel_hi:[1,0,1]
	v_pk_add_f32 v[110:111], v[110:111], 1.0 op_sel_hi:[1,0]
	v_pk_fma_f32 v[106:107], v[106:107], s[24:25], v[142:143] op_sel_hi:[1,0,1]
	v_rcp_f32_e32 v110, v110
	v_rcp_f32_e32 v111, v111
	v_ashrrev_i32_e32 v139, 31, v138
	v_med3_f32 v122, v122, s19, v161
	v_med3_f32 v123, v123, s19, v161
	v_pk_mul_f32 v[124:125], v[124:125], v[126:127]
	v_med3_f32 v114, v114, s19, v161
	v_med3_f32 v115, v115, s19, v161
	v_pk_mul_f32 v[116:117], v[116:117], v[118:119]
	v_med3_f32 v106, v106, s19, v161
	v_med3_f32 v107, v107, s19, v161
	v_pk_mul_f32 v[108:109], v[108:109], v[110:111]
	v_lshlrev_b64 v[104:105], 10, v[138:139]
	v_ashrrev_i32_e32 v137, 31, v136
	v_pk_mul_f32 v[122:123], v[122:123], v[124:125]
	v_pk_mul_f32 v[114:115], v[114:115], v[116:117]
	v_pk_mul_f32 v[106:107], v[106:107], v[108:109]
	v_lshl_add_u64 v[104:105], s[16:17], 0, v[104:105]
	v_pk_fma_f32 v[100:101], v[100:101], s[48:49], v[52:53] op_sel_hi:[1,0,1]
	v_cvt_pk_fp8_f32 v129, v122, v123 op_sel:[0,0,1]
	v_cvt_pk_fp8_f32 v130, v114, v115 op_sel:[0,0,1]
	v_cvt_pk_fp8_f32 v131, v106, v107 op_sel:[0,0,1]
	v_lshl_add_u64 v[104:105], v[104:105], 0, v[136:137]
	v_min_f32_e32 v100, 0x40e00000, v100
	v_min_f32_e32 v101, 0x40e00000, v101
	s_nop 1
	v_permlane16_swap_b32 v128, v130
	s_nop 1
	v_permlane16_swap_b32 v129, v131
	global_store_dwordx4 v[104:105], v[128:131], off
	v_pk_mul_f32 v[104:105], v[100:101], s[30:31] op_sel_hi:[1,0]
	v_pk_fma_f32 v[96:97], v[96:97], s[24:25], v[146:147] op_sel_hi:[1,0,1]
	v_exp_f32_e32 v104, v104
	v_exp_f32_e32 v105, v105
	v_pk_fma_f32 v[102:103], v[102:103], s[48:49], v[54:55] op_sel_hi:[1,0,1]
	v_med3_f32 v96, v96, s19, v161
	v_med3_f32 v97, v97, s19, v161
	v_pk_add_f32 v[104:105], v[104:105], 1.0 op_sel_hi:[1,0]
	v_pk_fma_f32 v[98:99], v[98:99], s[24:25], v[144:145] op_sel_hi:[1,0,1]
	v_rcp_f32_e32 v104, v104
	v_rcp_f32_e32 v105, v105
	v_med3_f32 v98, v98, s19, v161
	v_med3_f32 v99, v99, s19, v161
	v_pk_fma_f32 v[92:93], v[92:93], s[48:49], v[40:41] op_sel_hi:[1,0,1]
	v_pk_mul_f32 v[100:101], v[100:101], v[104:105]
	v_min_f32_e32 v92, 0x40e00000, v92
	v_pk_mul_f32 v[100:101], v[96:97], v[100:101]
	v_min_f32_e32 v96, 0x40e00000, v102
	v_min_f32_e32 v97, 0x40e00000, v103
	v_pk_mul_f32 v[102:103], v[96:97], s[30:31] op_sel_hi:[1,0]
	v_min_f32_e32 v93, 0x40e00000, v93
	v_exp_f32_e32 v102, v102
	v_exp_f32_e32 v103, v103
	v_pk_fma_f32 v[88:89], v[88:89], s[24:25], v[140:141] op_sel_hi:[1,0,1]
	v_pk_fma_f32 v[84:85], v[84:85], s[48:49], v[52:53] op_sel_hi:[1,0,1]
	v_med3_f32 v88, v88, s19, v161
	v_pk_add_f32 v[102:103], v[102:103], 1.0 op_sel_hi:[1,0]
	v_med3_f32 v89, v89, s19, v161
	v_rcp_f32_e32 v102, v102
	v_rcp_f32_e32 v103, v103
	v_min_f32_e32 v84, 0x40e00000, v84
	v_min_f32_e32 v85, 0x40e00000, v85
	v_pk_fma_f32 v[80:81], v[80:81], s[24:25], v[146:147] op_sel_hi:[1,0,1]
	v_pk_mul_f32 v[96:97], v[96:97], v[102:103]
	v_med3_f32 v80, v80, s19, v161
	v_pk_mul_f32 v[98:99], v[98:99], v[96:97]
	v_mov_b32_e32 v96, v185
	v_cvt_pk_fp8_f32 v96, v100, v101
	v_mov_b32_e32 v97, v185
	v_med3_f32 v81, v81, s19, v161
	v_pk_fma_f32 v[76:77], v[76:77], s[48:49], v[40:41] op_sel_hi:[1,0,1]
	v_cvt_pk_fp8_f32 v96, v98, v99 op_sel:[0,0,1]
	v_pk_mul_f32 v[98:99], v[92:93], s[30:31] op_sel_hi:[1,0]
	v_min_f32_e32 v76, 0x40e00000, v76
	v_exp_f32_e32 v98, v98
	v_exp_f32_e32 v99, v99
	v_min_f32_e32 v77, 0x40e00000, v77
	v_pk_fma_f32 v[72:73], v[72:73], s[24:25], v[140:141] op_sel_hi:[1,0,1]
	v_pk_fma_f32 v[78:79], v[78:79], s[48:49], v[42:43] op_sel_hi:[1,0,1]
	v_pk_add_f32 v[98:99], v[98:99], 1.0 op_sel_hi:[1,0]
	v_med3_f32 v72, v72, s19, v161
	v_rcp_f32_e32 v98, v98
	v_rcp_f32_e32 v99, v99
	v_med3_f32 v73, v73, s19, v161
	v_pk_fma_f32 v[74:75], v[74:75], s[24:25], v[142:143] op_sel_hi:[1,0,1]
	v_pk_fma_f32 v[68:69], v[68:69], s[48:49], v[52:53] op_sel_hi:[1,0,1]
	v_pk_mul_f32 v[92:93], v[92:93], v[98:99]
	v_mov_b32_e32 v98, v185
	v_pk_mul_f32 v[88:89], v[88:89], v[92:93]
	v_mov_b32_e32 v99, v185
	v_cvt_pk_fp8_f32 v97, v88, v89
	v_pk_mul_f32 v[88:89], v[84:85], s[30:31] op_sel_hi:[1,0]
	v_med3_f32 v74, v74, s19, v161
	v_exp_f32_e32 v88, v88
	v_exp_f32_e32 v89, v89
	v_med3_f32 v75, v75, s19, v161
	v_min_f32_e32 v68, 0x40e00000, v68
	v_min_f32_e32 v69, 0x40e00000, v69
	v_pk_add_f32 v[88:89], v[88:89], 1.0 op_sel_hi:[1,0]
	v_pk_fma_f32 v[64:65], v[64:65], s[24:25], v[146:147] op_sel_hi:[1,0,1]
	v_rcp_f32_e32 v88, v88
	v_rcp_f32_e32 v89, v89
	v_pk_fma_f32 v[70:71], v[70:71], s[48:49], v[54:55] op_sel_hi:[1,0,1]
	v_med3_f32 v64, v64, s19, v161
	v_med3_f32 v65, v65, s19, v161
	v_pk_mul_f32 v[84:85], v[84:85], v[88:89]
	v_pk_fma_f32 v[66:67], v[66:67], s[24:25], v[144:145] op_sel_hi:[1,0,1]
	v_pk_mul_f32 v[80:81], v[80:81], v[84:85]
	v_med3_f32 v66, v66, s19, v161
	v_cvt_pk_fp8_f32 v98, v80, v81
	v_pk_mul_f32 v[80:81], v[76:77], s[30:31] op_sel_hi:[1,0]
	v_med3_f32 v67, v67, s19, v161
	v_exp_f32_e32 v80, v80
	v_exp_f32_e32 v81, v81
	v_pk_fma_f32 v[60:61], v[60:61], s[48:49], v[40:41] op_sel_hi:[1,0,1]
	v_pk_fma_f32 v[56:57], v[56:57], s[24:25], v[140:141] op_sel_hi:[1,0,1]
	v_min_f32_e32 v60, 0x40e00000, v60
	v_pk_add_f32 v[80:81], v[80:81], 1.0 op_sel_hi:[1,0]
	v_min_f32_e32 v61, 0x40e00000, v61
	v_rcp_f32_e32 v80, v80
	v_rcp_f32_e32 v81, v81
	v_med3_f32 v56, v56, s19, v161
	v_med3_f32 v57, v57, s19, v161
	v_pk_fma_f32 v[48:49], v[48:49], s[48:49], v[52:53] op_sel_hi:[1,0,1]
	v_pk_mul_f32 v[76:77], v[76:77], v[80:81]
	v_min_f32_e32 v48, 0x40e00000, v48
	v_pk_mul_f32 v[72:73], v[72:73], v[76:77]
	v_min_f32_e32 v76, 0x40e00000, v78
	v_min_f32_e32 v77, 0x40e00000, v79
	v_pk_mul_f32 v[78:79], v[76:77], s[30:31] op_sel_hi:[1,0]
	v_cvt_pk_fp8_f32 v99, v72, v73
	v_exp_f32_e32 v78, v78
	v_exp_f32_e32 v79, v79
	v_min_f32_e32 v49, 0x40e00000, v49
	v_pk_fma_f32 v[44:45], v[44:45], s[24:25], v[146:147] op_sel_hi:[1,0,1]
	v_pk_fma_f32 v[36:37], v[36:37], s[48:49], v[40:41] op_sel_hi:[1,0,1]
	v_pk_add_f32 v[78:79], v[78:79], 1.0 op_sel_hi:[1,0]
	v_med3_f32 v44, v44, s19, v161
	v_rcp_f32_e32 v78, v78
	v_rcp_f32_e32 v79, v79
	v_med3_f32 v45, v45, s19, v161
	v_min_f32_e32 v36, 0x40e00000, v36
	v_min_f32_e32 v37, 0x40e00000, v37
	v_pk_mul_f32 v[76:77], v[76:77], v[78:79]
	v_pk_fma_f32 v[94:95], v[94:95], s[48:49], v[42:43] op_sel_hi:[1,0,1]
	v_pk_mul_f32 v[74:75], v[74:75], v[76:77]
	v_pk_fma_f32 v[86:87], v[86:87], s[48:49], v[54:55] op_sel_hi:[1,0,1]
	v_cvt_pk_fp8_f32 v99, v74, v75 op_sel:[0,0,1]
	v_pk_mul_f32 v[74:75], v[68:69], s[30:31] op_sel_hi:[1,0]
	v_min_f32_e32 v92, 0x40e00000, v94
	v_exp_f32_e32 v74, v74
	v_exp_f32_e32 v75, v75
	v_min_f32_e32 v93, 0x40e00000, v95
	v_min_f32_e32 v84, 0x40e00000, v86
	v_min_f32_e32 v85, 0x40e00000, v87
	v_pk_add_f32 v[74:75], v[74:75], 1.0 op_sel_hi:[1,0]
	v_pk_mul_f32 v[94:95], v[92:93], s[30:31] op_sel_hi:[1,0]
	v_rcp_f32_e32 v74, v74
	v_rcp_f32_e32 v75, v75
	v_pk_mul_f32 v[86:87], v[84:85], s[30:31] op_sel_hi:[1,0]
	v_exp_f32_e32 v94, v94
	v_exp_f32_e32 v95, v95
	v_pk_mul_f32 v[68:69], v[68:69], v[74:75]
	v_exp_f32_e32 v86, v86
	v_pk_mul_f32 v[68:69], v[64:65], v[68:69]
	v_min_f32_e32 v64, 0x40e00000, v70
	v_min_f32_e32 v65, 0x40e00000, v71
	v_pk_mul_f32 v[70:71], v[64:65], s[30:31] op_sel_hi:[1,0]
	v_exp_f32_e32 v87, v87
	v_exp_f32_e32 v70, v70
	v_exp_f32_e32 v71, v71
	v_pk_fma_f32 v[32:33], v[32:33], s[24:25], v[140:141] op_sel_hi:[1,0,1]
	v_pk_fma_f32 v[62:63], v[62:63], s[48:49], v[42:43] op_sel_hi:[1,0,1]
	v_pk_fma_f32 v[50:51], v[50:51], s[48:49], v[54:55] op_sel_hi:[1,0,1]
	v_pk_add_f32 v[70:71], v[70:71], 1.0 op_sel_hi:[1,0]
	v_pk_fma_f32 v[38:39], v[38:39], s[48:49], v[42:43] op_sel_hi:[1,0,1]
	v_rcp_f32_e32 v70, v70
	v_rcp_f32_e32 v71, v71
	v_med3_f32 v32, v32, s19, v161
	v_med3_f32 v33, v33, s19, v161
	v_pk_add_f32 v[94:95], v[94:95], 1.0 op_sel_hi:[1,0]
	v_pk_mul_f32 v[64:65], v[64:65], v[70:71]
	v_pk_add_f32 v[86:87], v[86:87], 1.0 op_sel_hi:[1,0]
	v_pk_mul_f32 v[66:67], v[66:67], v[64:65]
	v_mov_b32_e32 v64, v185
	v_cvt_pk_fp8_f32 v64, v68, v69
	v_mov_b32_e32 v65, v185
	v_rcp_f32_e32 v94, v94
	v_rcp_f32_e32 v95, v95
	v_cvt_pk_fp8_f32 v64, v66, v67 op_sel:[0,0,1]
	v_pk_mul_f32 v[66:67], v[60:61], s[30:31] op_sel_hi:[1,0]
	v_rcp_f32_e32 v86, v86
	v_exp_f32_e32 v66, v66
	v_exp_f32_e32 v67, v67
	v_rcp_f32_e32 v87, v87
	v_or_b32_e32 v72, 32, v138
	v_pk_fma_f32 v[90:91], v[90:91], s[24:25], v[142:143] op_sel_hi:[1,0,1]
	v_pk_add_f32 v[66:67], v[66:67], 1.0 op_sel_hi:[1,0]
	v_pk_fma_f32 v[82:83], v[82:83], s[24:25], v[144:145] op_sel_hi:[1,0,1]
	v_rcp_f32_e32 v66, v66
	v_rcp_f32_e32 v67, v67
	v_ashrrev_i32_e32 v73, 31, v72
	v_med3_f32 v90, v90, s19, v161
	v_med3_f32 v91, v91, s19, v161
	v_pk_mul_f32 v[60:61], v[60:61], v[66:67]
	v_mov_b32_e32 v66, v185
	v_pk_mul_f32 v[56:57], v[56:57], v[60:61]
	v_min_f32_e32 v60, 0x40e00000, v62
	v_cvt_pk_fp8_f32 v65, v56, v57
	v_pk_mul_f32 v[56:57], v[48:49], s[30:31] op_sel_hi:[1,0]
	v_min_f32_e32 v61, 0x40e00000, v63
	v_exp_f32_e32 v56, v56
	v_exp_f32_e32 v57, v57
	v_pk_mul_f32 v[62:63], v[60:61], s[30:31] op_sel_hi:[1,0]
	v_pk_mul_f32 v[92:93], v[92:93], v[94:95]
	v_exp_f32_e32 v62, v62
	v_pk_add_f32 v[56:57], v[56:57], 1.0 op_sel_hi:[1,0]
	v_exp_f32_e32 v63, v63
	v_rcp_f32_e32 v56, v56
	v_rcp_f32_e32 v57, v57
	v_med3_f32 v82, v82, s19, v161
	v_med3_f32 v83, v83, s19, v161
	v_pk_mul_f32 v[84:85], v[84:85], v[86:87]
	v_pk_mul_f32 v[48:49], v[48:49], v[56:57]
	v_lshlrev_b64 v[72:73], 10, v[72:73]
	v_pk_mul_f32 v[44:45], v[44:45], v[48:49]
	v_min_f32_e32 v48, 0x40e00000, v50
	v_cvt_pk_fp8_f32 v66, v44, v45
	v_pk_mul_f32 v[44:45], v[36:37], s[30:31] op_sel_hi:[1,0]
	v_min_f32_e32 v49, 0x40e00000, v51
	v_exp_f32_e32 v44, v44
	v_exp_f32_e32 v45, v45
	v_pk_mul_f32 v[50:51], v[48:49], s[30:31] op_sel_hi:[1,0]
	v_pk_add_f32 v[62:63], v[62:63], 1.0 op_sel_hi:[1,0]
	v_exp_f32_e32 v50, v50
	v_pk_add_f32 v[44:45], v[44:45], 1.0 op_sel_hi:[1,0]
	v_exp_f32_e32 v51, v51
	v_rcp_f32_e32 v44, v44
	v_rcp_f32_e32 v45, v45
	v_pk_mul_f32 v[90:91], v[90:91], v[92:93]
	v_pk_add_f32 v[50:51], v[50:51], 1.0 op_sel_hi:[1,0]
	v_pk_mul_f32 v[82:83], v[82:83], v[84:85]
	v_pk_mul_f32 v[36:37], v[36:37], v[44:45]
	v_lshl_add_u64 v[72:73], s[16:17], 0, v[72:73]
	v_pk_mul_f32 v[32:33], v[32:33], v[36:37]
	v_min_f32_e32 v36, 0x40e00000, v38
	v_min_f32_e32 v37, 0x40e00000, v39
	v_pk_mul_f32 v[38:39], v[36:37], s[30:31] op_sel_hi:[1,0]
	v_rcp_f32_e32 v62, v62
	v_exp_f32_e32 v38, v38
	v_exp_f32_e32 v39, v39
	v_rcp_f32_e32 v63, v63
	v_rcp_f32_e32 v50, v50
	v_rcp_f32_e32 v51, v51
	v_pk_add_f32 v[38:39], v[38:39], 1.0 op_sel_hi:[1,0]
	v_cvt_pk_fp8_f32 v97, v90, v91 op_sel:[0,0,1]
	v_rcp_f32_e32 v38, v38
	v_rcp_f32_e32 v39, v39
	v_cvt_pk_fp8_f32 v98, v82, v83 op_sel:[0,0,1]
	v_lshl_add_u64 v[72:73], v[72:73], 0, v[136:137]
	v_mov_b32_e32 v67, v185
	s_nop 1
	v_permlane16_swap_b32 v96, v98
	s_nop 1
	v_permlane16_swap_b32 v97, v99
	global_store_dwordx4 v[72:73], v[96:99], off
	v_add_u32_e32 v72, 0x80, v138
	v_cvt_pk_fp8_f32 v67, v32, v33
	v_pk_fma_f32 v[58:59], v[58:59], s[24:25], v[142:143] op_sel_hi:[1,0,1]
	v_pk_fma_f32 v[46:47], v[46:47], s[24:25], v[144:145] op_sel_hi:[1,0,1]
	v_pk_fma_f32 v[34:35], v[34:35], s[24:25], v[142:143] op_sel_hi:[1,0,1]
	v_ashrrev_i32_e32 v73, 31, v72
	v_med3_f32 v58, v58, s19, v161
	v_med3_f32 v59, v59, s19, v161
	v_pk_mul_f32 v[60:61], v[60:61], v[62:63]
	v_med3_f32 v46, v46, s19, v161
	v_med3_f32 v47, v47, s19, v161
	v_pk_mul_f32 v[48:49], v[48:49], v[50:51]
	v_med3_f32 v34, v34, s19, v161
	v_med3_f32 v35, v35, s19, v161
	v_pk_mul_f32 v[36:37], v[36:37], v[38:39]
	v_lshlrev_b64 v[32:33], 10, v[72:73]
	v_pk_mul_f32 v[58:59], v[58:59], v[60:61]
	v_pk_mul_f32 v[46:47], v[46:47], v[48:49]
	v_pk_mul_f32 v[34:35], v[34:35], v[36:37]
	v_lshl_add_u64 v[32:33], s[16:17], 0, v[32:33]
	v_pk_fma_f32 v[28:29], v[28:29], s[48:49], v[52:53] op_sel_hi:[1,0,1]
	v_cvt_pk_fp8_f32 v65, v58, v59 op_sel:[0,0,1]
	v_cvt_pk_fp8_f32 v66, v46, v47 op_sel:[0,0,1]
	v_cvt_pk_fp8_f32 v67, v34, v35 op_sel:[0,0,1]
	v_lshl_add_u64 v[32:33], v[32:33], 0, v[136:137]
	v_min_f32_e32 v28, 0x40e00000, v28
	v_min_f32_e32 v29, 0x40e00000, v29
	s_nop 1
	v_permlane16_swap_b32 v64, v66
	s_nop 1
	v_permlane16_swap_b32 v65, v67
	global_store_dwordx4 v[32:33], v[64:67], off
	v_pk_mul_f32 v[32:33], v[28:29], s[30:31] op_sel_hi:[1,0]
	v_pk_fma_f32 v[24:25], v[24:25], s[24:25], v[146:147] op_sel_hi:[1,0,1]
	v_exp_f32_e32 v32, v32
	v_exp_f32_e32 v33, v33
	v_pk_fma_f32 v[30:31], v[30:31], s[48:49], v[54:55] op_sel_hi:[1,0,1]
	v_med3_f32 v24, v24, s19, v161
	v_med3_f32 v25, v25, s19, v161
	v_pk_add_f32 v[32:33], v[32:33], 1.0 op_sel_hi:[1,0]
	v_pk_fma_f32 v[26:27], v[26:27], s[24:25], v[144:145] op_sel_hi:[1,0,1]
	v_rcp_f32_e32 v32, v32
	v_rcp_f32_e32 v33, v33
	v_med3_f32 v26, v26, s19, v161
	v_med3_f32 v27, v27, s19, v161
	v_pk_fma_f32 v[20:21], v[20:21], s[48:49], v[40:41] op_sel_hi:[1,0,1]
	v_pk_mul_f32 v[28:29], v[28:29], v[32:33]
	v_min_f32_e32 v20, 0x40e00000, v20
	v_pk_mul_f32 v[28:29], v[24:25], v[28:29]
	v_min_f32_e32 v24, 0x40e00000, v30
	v_min_f32_e32 v25, 0x40e00000, v31
	v_pk_mul_f32 v[30:31], v[24:25], s[30:31] op_sel_hi:[1,0]
	v_min_f32_e32 v21, 0x40e00000, v21
	v_exp_f32_e32 v30, v30
	v_exp_f32_e32 v31, v31
	v_pk_fma_f32 v[16:17], v[16:17], s[24:25], v[140:141] op_sel_hi:[1,0,1]
	v_pk_fma_f32 v[12:13], v[12:13], s[48:49], v[52:53] op_sel_hi:[1,0,1]
	v_med3_f32 v16, v16, s19, v161
	v_pk_add_f32 v[30:31], v[30:31], 1.0 op_sel_hi:[1,0]
	v_med3_f32 v17, v17, s19, v161
	v_rcp_f32_e32 v30, v30
	v_rcp_f32_e32 v31, v31
	v_min_f32_e32 v12, 0x40e00000, v12
	v_min_f32_e32 v13, 0x40e00000, v13
	v_pk_fma_f32 v[8:9], v[8:9], s[24:25], v[146:147] op_sel_hi:[1,0,1]
	v_pk_mul_f32 v[24:25], v[24:25], v[30:31]
	v_med3_f32 v8, v8, s19, v161
	v_pk_mul_f32 v[26:27], v[26:27], v[24:25]
	v_mov_b32_e32 v24, v185
	v_cvt_pk_fp8_f32 v24, v28, v29
	v_mov_b32_e32 v25, v185
	v_med3_f32 v9, v9, s19, v161
	v_pk_fma_f32 v[4:5], v[4:5], s[48:49], v[40:41] op_sel_hi:[1,0,1]
	v_cvt_pk_fp8_f32 v24, v26, v27 op_sel:[0,0,1]
	v_pk_mul_f32 v[26:27], v[20:21], s[30:31] op_sel_hi:[1,0]
	v_min_f32_e32 v4, 0x40e00000, v4
	v_exp_f32_e32 v26, v26
	v_exp_f32_e32 v27, v27
	v_min_f32_e32 v5, 0x40e00000, v5
	v_pk_fma_f32 v[0:1], v[0:1], s[24:25], v[140:141] op_sel_hi:[1,0,1]
	v_pk_fma_f32 v[22:23], v[22:23], s[48:49], v[42:43] op_sel_hi:[1,0,1]
	v_pk_add_f32 v[26:27], v[26:27], 1.0 op_sel_hi:[1,0]
	v_pk_fma_f32 v[14:15], v[14:15], s[48:49], v[54:55] op_sel_hi:[1,0,1]
	v_rcp_f32_e32 v26, v26
	v_rcp_f32_e32 v27, v27
	v_pk_fma_f32 v[6:7], v[6:7], s[48:49], v[42:43] op_sel_hi:[1,0,1]
	v_med3_f32 v0, v0, s19, v161
	v_med3_f32 v1, v1, s19, v161
	v_pk_mul_f32 v[20:21], v[20:21], v[26:27]
	v_mov_b32_e32 v26, v185
	v_pk_mul_f32 v[16:17], v[16:17], v[20:21]
	v_min_f32_e32 v20, 0x40e00000, v22
	v_cvt_pk_fp8_f32 v25, v16, v17
	v_pk_mul_f32 v[16:17], v[12:13], s[30:31] op_sel_hi:[1,0]
	v_min_f32_e32 v21, 0x40e00000, v23
	v_exp_f32_e32 v16, v16
	v_exp_f32_e32 v17, v17
	v_pk_mul_f32 v[22:23], v[20:21], s[30:31] op_sel_hi:[1,0]
	v_mov_b32_e32 v27, v185
	v_exp_f32_e32 v22, v22
	v_pk_add_f32 v[16:17], v[16:17], 1.0 op_sel_hi:[1,0]
	v_exp_f32_e32 v23, v23
	v_rcp_f32_e32 v16, v16
	v_rcp_f32_e32 v17, v17
	v_pk_fma_f32 v[18:19], v[18:19], s[24:25], v[142:143] op_sel_hi:[1,0,1]
	v_pk_add_f32 v[22:23], v[22:23], 1.0 op_sel_hi:[1,0]
	v_pk_fma_f32 v[10:11], v[10:11], s[24:25], v[144:145] op_sel_hi:[1,0,1]
	v_pk_mul_f32 v[12:13], v[12:13], v[16:17]
	v_rcp_f32_e32 v22, v22
	v_pk_mul_f32 v[8:9], v[8:9], v[12:13]
	v_min_f32_e32 v12, 0x40e00000, v14
	v_cvt_pk_fp8_f32 v26, v8, v9
	v_pk_mul_f32 v[8:9], v[4:5], s[30:31] op_sel_hi:[1,0]
	v_min_f32_e32 v13, 0x40e00000, v15
	v_exp_f32_e32 v8, v8
	v_exp_f32_e32 v9, v9
	v_pk_mul_f32 v[14:15], v[12:13], s[30:31] op_sel_hi:[1,0]
	v_rcp_f32_e32 v23, v23
	v_exp_f32_e32 v14, v14
	v_pk_add_f32 v[8:9], v[8:9], 1.0 op_sel_hi:[1,0]
	v_exp_f32_e32 v15, v15
	v_rcp_f32_e32 v8, v8
	v_rcp_f32_e32 v9, v9
	v_pk_fma_f32 v[2:3], v[2:3], s[24:25], v[142:143] op_sel_hi:[1,0,1]
	v_pk_add_f32 v[14:15], v[14:15], 1.0 op_sel_hi:[1,0]
	v_med3_f32 v18, v18, s19, v161
	v_pk_mul_f32 v[4:5], v[4:5], v[8:9]
	v_rcp_f32_e32 v14, v14
	v_pk_mul_f32 v[0:1], v[0:1], v[4:5]
	v_min_f32_e32 v4, 0x40e00000, v6
	v_min_f32_e32 v5, 0x40e00000, v7
	v_pk_mul_f32 v[6:7], v[4:5], s[30:31] op_sel_hi:[1,0]
	v_rcp_f32_e32 v15, v15
	v_exp_f32_e32 v6, v6
	v_exp_f32_e32 v7, v7
	v_cvt_pk_fp8_f32 v27, v0, v1
	v_add_u32_e32 v0, 0xa0, v138
	v_ashrrev_i32_e32 v1, 31, v0
	v_pk_add_f32 v[6:7], v[6:7], 1.0 op_sel_hi:[1,0]
	v_med3_f32 v19, v19, s19, v161
	v_rcp_f32_e32 v6, v6
	v_rcp_f32_e32 v7, v7
	v_pk_mul_f32 v[20:21], v[20:21], v[22:23]
	v_med3_f32 v10, v10, s19, v161
	v_med3_f32 v11, v11, s19, v161
	v_pk_mul_f32 v[12:13], v[12:13], v[14:15]
	v_med3_f32 v2, v2, s19, v161
	v_med3_f32 v3, v3, s19, v161
	v_pk_mul_f32 v[4:5], v[4:5], v[6:7]
	v_lshlrev_b64 v[0:1], 10, v[0:1]
	v_pk_mul_f32 v[18:19], v[18:19], v[20:21]
	v_pk_mul_f32 v[10:11], v[10:11], v[12:13]
	v_pk_mul_f32 v[2:3], v[2:3], v[4:5]
	v_lshl_add_u64 v[0:1], s[16:17], 0, v[0:1]
	v_cvt_pk_fp8_f32 v25, v18, v19 op_sel:[0,0,1]
	v_cvt_pk_fp8_f32 v26, v10, v11 op_sel:[0,0,1]
	v_cvt_pk_fp8_f32 v27, v2, v3 op_sel:[0,0,1]
	v_lshl_add_u64 v[0:1], v[0:1], 0, v[136:137]
	s_mov_b64 s[24:25], -1
	s_and_b64 vcc, exec, s[2:3]
	s_nop 1
	v_permlane16_swap_b32 v24, v26
	s_nop 1
	v_permlane16_swap_b32 v25, v27
	global_store_dwordx4 v[0:1], v[24:27], off
	s_cbranch_vccnz .LBB0_1031
	v_mov_b32_e32 v0, v185
	v_mov_b32_e32 v1, v185
	s_andn2_b64 vcc, exec, s[8:9]
	s_waitcnt vmcnt(4)
	s_cbranch_vccnz .LBB0_1044
	v_max_i32_e32 v1, 0, v156
	v_max_i32_e32 v2, 0, v157
	v_lshrrev_b32_e32 v1, 2, v1
	v_lshlrev_b32_e32 v2, 14, v2
	v_and_or_b32 v1, v2, s45, v1
	v_mbcnt_lo_u32_b32 v2, -1, 0
	v_mbcnt_hi_u32_b32 v2, -1, v2
	s_mov_b32 s2, s61
	v_lshlrev_b32_e32 v2, 3, v2
	v_readfirstlane_b32 s18, v155
	v_lshl_or_b32 v2, s2, 9, v2
	v_add_u32_e32 v2, s74, v2
	ds_write_b32 v2, v1
	v_max_i32_e32 v1, 0, v158
	v_max_i32_e32 v2, 0, v159
	v_lshrrev_b32_e32 v1, 2, v1
	v_lshlrev_b32_e32 v2, 14, v2
	v_and_or_b32 v1, v2, s45, v1
	v_mbcnt_lo_u32_b32 v2, -1, 0
	v_mbcnt_hi_u32_b32 v2, -1, v2
	s_mov_b32 s2, s61
	v_lshlrev_b32_e32 v2, 3, v2
	s_nop 0
	v_lshl_or_b32 v2, s2, 9, v2
	v_add_u32_e32 v2, s74, v2
	ds_write_b32 v2, v1 offset:4
